# GEMM K-loops: MFMA blocks start right behind the barrier (priority raise moved in front of it, the duplicate lgkmcnt(0) behind it dropped)
# baseline (speedup 1.0000x reference)
.LBB0_398:
	s_add_u32 s48, s46, 0xfff80080
	s_addc_u32 s49, s47, -1
	s_add_i32 s68, 0, 0x10000
	s_cmp_eq_u32 s67, 28
	s_cselect_b32 s53, s10, s49
	s_cselect_b32 s52, s11, s48
	s_cselect_b32 s49, s39, s66
	s_cselect_b32 s48, s41, s65
	s_add_i32 s70, 0, 0x14000
	ds_read_b128 v[146:149], v142
	ds_read_b128 v[150:153], v142 offset:1024
	ds_read_b128 v[154:157], v142 offset:2048
	ds_read_b128 v[158:161], v142 offset:3072
	ds_read_b128 v[162:165], v142 offset:16384
	ds_read_b128 v[166:169], v142 offset:17408
	ds_read_b128 v[170:173], v142 offset:18432
	ds_read_b128 v[178:181], v142 offset:19456
	v_lshl_add_u64 v[174:175], s[46:47], 0, v[138:139]
	s_add_i32 m0, s56, 0xc000
	ds_read_b128 v[182:185], v145
	ds_read_b128 v[186:189], v145 offset:1024
	ds_read_b128 v[190:193], v145 offset:2048
	ds_read_b128 v[194:197], v145 offset:3072
	ds_read_b128 v[198:201], v145 offset:4096
	ds_read_b128 v[202:205], v145 offset:5120
	ds_read_b128 v[206:209], v145 offset:6144
	ds_read_b128 v[226:229], v145 offset:7168
	global_load_lds_dwordx4 v[174:175], off
	v_lshl_add_u64 v[174:175], s[46:47], 0, v[140:141]
	s_add_i32 m0, s56, 0xe000
	s_nop 0
	global_load_lds_dwordx4 v[174:175], off
	s_waitcnt vmcnt(8)
	s_waitcnt lgkmcnt(0)
	s_setprio 1
	s_barrier
	v_mfma_f32_16x16x32_bf16 v[128:131], v[146:149], v[182:185], v[128:131]
	v_mfma_f32_16x16x32_bf16 v[124:127], v[154:157], v[182:185], v[124:127]
	v_mfma_f32_16x16x32_bf16 v[120:123], v[146:149], v[190:193], v[120:123]
	v_mfma_f32_16x16x32_bf16 v[116:119], v[154:157], v[190:193], v[116:119]
	v_mfma_f32_16x16x32_bf16 v[104:107], v[146:149], v[198:201], v[104:107]
	v_mfma_f32_16x16x32_bf16 v[100:103], v[154:157], v[198:201], v[100:103]
	v_mfma_f32_16x16x32_bf16 v[88:91], v[146:149], v[206:209], v[88:91]
	v_mfma_f32_16x16x32_bf16 v[84:87], v[154:157], v[206:209], v[84:87]
	v_mfma_f32_16x16x32_bf16 v[128:131], v[150:153], v[186:189], v[128:131]
	v_mfma_f32_16x16x32_bf16 v[124:127], v[158:161], v[186:189], v[124:127]
	v_mfma_f32_16x16x32_bf16 v[120:123], v[150:153], v[194:197], v[120:123]
	v_mfma_f32_16x16x32_bf16 v[116:119], v[158:161], v[194:197], v[116:119]
	v_mfma_f32_16x16x32_bf16 v[104:107], v[150:153], v[202:205], v[104:107]
	v_mfma_f32_16x16x32_bf16 v[100:103], v[158:161], v[202:205], v[100:103]
	v_mfma_f32_16x16x32_bf16 v[88:91], v[150:153], v[226:229], v[88:91]
	v_mfma_f32_16x16x32_bf16 v[84:87], v[158:161], v[226:229], v[84:87]
	s_setprio 0
	s_setprio 1
	v_mfma_f32_16x16x32_bf16 v[112:115], v[162:165], v[182:185], v[112:115]
	v_mfma_f32_16x16x32_bf16 v[108:111], v[170:173], v[182:185], v[108:111]
	v_mfma_f32_16x16x32_bf16 v[96:99], v[162:165], v[190:193], v[96:99]
	v_mfma_f32_16x16x32_bf16 v[92:95], v[170:173], v[190:193], v[92:95]
	v_mfma_f32_16x16x32_bf16 v[80:83], v[162:165], v[198:201], v[80:83]
	v_mfma_f32_16x16x32_bf16 v[76:79], v[170:173], v[198:201], v[76:79]
	v_mfma_f32_16x16x32_bf16 v[72:75], v[162:165], v[206:209], v[72:75]
	v_mfma_f32_16x16x32_bf16 v[68:71], v[170:173], v[206:209], v[68:71]
	v_mfma_f32_16x16x32_bf16 v[112:115], v[166:169], v[186:189], v[112:115]
	v_mfma_f32_16x16x32_bf16 v[108:111], v[178:181], v[186:189], v[108:111]
	v_mfma_f32_16x16x32_bf16 v[96:99], v[166:169], v[194:197], v[96:99]
	v_mfma_f32_16x16x32_bf16 v[92:95], v[178:181], v[194:197], v[92:95]
	v_mfma_f32_16x16x32_bf16 v[80:83], v[166:169], v[202:205], v[80:83]
	v_mfma_f32_16x16x32_bf16 v[76:79], v[178:181], v[202:205], v[76:79]
	v_mfma_f32_16x16x32_bf16 v[72:75], v[166:169], v[226:229], v[72:75]
	v_mfma_f32_16x16x32_bf16 v[68:71], v[178:181], v[226:229], v[68:71]
	s_setprio 0
	s_barrier
	s_add_i32 s68, s68, s55
	v_lshl_add_u64 v[174:175], s[48:49], 0, v[2:3]
	s_mov_b32 m0, s68
	ds_read_b128 v[182:185], v145 offset:16384
	ds_read_b128 v[186:189], v145 offset:17408
	ds_read_b128 v[190:193], v145 offset:18432
	ds_read_b128 v[194:197], v145 offset:19456
	ds_read_b128 v[198:201], v145 offset:20480
	ds_read_b128 v[202:205], v145 offset:21504
	ds_read_b128 v[206:209], v145 offset:22528
	ds_read_b128 v[226:229], v145 offset:23552
	global_load_lds_dwordx4 v[174:175], off
	s_add_i32 m0, s68, 0x2000
	s_add_u32 s68, s48, 0x80000
	v_lshl_add_u64 v[210:211], s[48:49], 0, v[132:133]
	s_addc_u32 s69, s49, 0
	s_add_i32 s70, s70, s55
	global_load_lds_dwordx4 v[210:211], off
	v_lshl_add_u64 v[214:215], s[68:69], 0, v[2:3]
	s_mov_b32 m0, s70
	v_lshl_add_u64 v[230:231], s[52:53], 0, v[134:135]
	global_load_lds_dwordx4 v[214:215], off
	v_lshl_add_u64 v[214:215], s[68:69], 0, v[132:133]
	s_add_i32 m0, s70, 0x2000
	s_nop 0
	global_load_lds_dwordx4 v[214:215], off
	v_lshl_add_u64 v[214:215], s[52:53], 0, v[136:137]
	s_mov_b32 m0, s56
	s_nop 0
	global_load_lds_dwordx4 v[214:215], off
	s_mov_b32 m0, s57
	s_nop 0
	global_load_lds_dwordx4 v[230:231], off
	s_waitcnt vmcnt(8)
	s_waitcnt lgkmcnt(0)
	s_setprio 1
	s_barrier
	v_mfma_f32_16x16x32_bf16 v[64:67], v[146:149], v[182:185], v[64:67]
	v_mfma_f32_16x16x32_bf16 v[60:63], v[154:157], v[182:185], v[60:63]
	v_mfma_f32_16x16x32_bf16 v[56:59], v[146:149], v[190:193], v[56:59]
	v_mfma_f32_16x16x32_bf16 v[52:55], v[154:157], v[190:193], v[52:55]
	v_mfma_f32_16x16x32_bf16 v[40:43], v[146:149], v[198:201], v[40:43]
	v_mfma_f32_16x16x32_bf16 v[36:39], v[154:157], v[198:201], v[36:39]
	v_mfma_f32_16x16x32_bf16 v[24:27], v[146:149], v[206:209], v[24:27]
	v_mfma_f32_16x16x32_bf16 v[20:23], v[154:157], v[206:209], v[20:23]
	v_mfma_f32_16x16x32_bf16 v[64:67], v[150:153], v[186:189], v[64:67]
	v_mfma_f32_16x16x32_bf16 v[60:63], v[158:161], v[186:189], v[60:63]
	v_mfma_f32_16x16x32_bf16 v[56:59], v[150:153], v[194:197], v[56:59]
	v_mfma_f32_16x16x32_bf16 v[52:55], v[158:161], v[194:197], v[52:55]
	v_mfma_f32_16x16x32_bf16 v[40:43], v[150:153], v[202:205], v[40:43]
	v_mfma_f32_16x16x32_bf16 v[36:39], v[158:161], v[202:205], v[36:39]
	v_mfma_f32_16x16x32_bf16 v[24:27], v[150:153], v[226:229], v[24:27]
	v_mfma_f32_16x16x32_bf16 v[20:23], v[158:161], v[226:229], v[20:23]
	s_setprio 0
	s_setprio 1
	v_mfma_f32_16x16x32_bf16 v[48:51], v[162:165], v[182:185], v[48:51]
	v_mfma_f32_16x16x32_bf16 v[44:47], v[170:173], v[182:185], v[44:47]
	v_mfma_f32_16x16x32_bf16 v[32:35], v[162:165], v[190:193], v[32:35]
	v_mfma_f32_16x16x32_bf16 v[28:31], v[170:173], v[190:193], v[28:31]
	v_mfma_f32_16x16x32_bf16 v[16:19], v[162:165], v[198:201], v[16:19]
	v_mfma_f32_16x16x32_bf16 v[12:15], v[170:173], v[198:201], v[12:15]
	v_mfma_f32_16x16x32_bf16 v[8:11], v[162:165], v[206:209], v[8:11]
	v_mfma_f32_16x16x32_bf16 v[4:7], v[170:173], v[206:209], v[4:7]
	v_mfma_f32_16x16x32_bf16 v[48:51], v[166:169], v[186:189], v[48:51]
	v_mfma_f32_16x16x32_bf16 v[44:47], v[178:181], v[186:189], v[44:47]
	v_mfma_f32_16x16x32_bf16 v[32:35], v[166:169], v[194:197], v[32:35]
	v_mfma_f32_16x16x32_bf16 v[28:31], v[178:181], v[194:197], v[28:31]
	v_mfma_f32_16x16x32_bf16 v[16:19], v[166:169], v[202:205], v[16:19]
	v_mfma_f32_16x16x32_bf16 v[12:15], v[178:181], v[202:205], v[12:15]
	v_mfma_f32_16x16x32_bf16 v[8:11], v[166:169], v[226:229], v[8:11]
	v_mfma_f32_16x16x32_bf16 v[4:7], v[178:181], v[226:229], v[4:7]
	s_setprio 0
	s_barrier
	s_add_i32 s68, 0, 0x18000
	s_add_i32 s69, 0, 0x1c000
	ds_read_b128 v[146:149], v142 offset:32768
	ds_read_b128 v[150:153], v142 offset:33792
	ds_read_b128 v[154:157], v142 offset:34816
	ds_read_b128 v[158:161], v142 offset:35840
	ds_read_b128 v[162:165], v142 offset:49152
	ds_read_b128 v[166:169], v142 offset:50176
	ds_read_b128 v[170:173], v142 offset:51200
	ds_read_b128 v[178:181], v142 offset:52224
	s_add_u32 s52, s52, 0x80000
	s_addc_u32 s53, s53, 0
	s_mov_b32 m0, s58
	v_lshl_add_u64 v[232:233], s[52:53], 0, v[136:137]
	ds_read_b128 v[182:185], v145 offset:32768
	ds_read_b128 v[186:189], v145 offset:33792
	ds_read_b128 v[190:193], v145 offset:34816
	ds_read_b128 v[194:197], v145 offset:35840
	ds_read_b128 v[198:201], v145 offset:36864
	ds_read_b128 v[202:205], v145 offset:37888
	ds_read_b128 v[206:209], v145 offset:38912
	ds_read_b128 v[226:229], v145 offset:39936
	global_load_lds_dwordx4 v[232:233], off
	v_lshl_add_u64 v[232:233], s[52:53], 0, v[134:135]
	s_mov_b32 m0, s59
	s_nop 0
	global_load_lds_dwordx4 v[232:233], off
	s_waitcnt vmcnt(8)
	s_waitcnt lgkmcnt(0)
	s_setprio 1
	s_barrier
	v_mfma_f32_16x16x32_bf16 v[128:131], v[146:149], v[182:185], v[128:131]
	v_mfma_f32_16x16x32_bf16 v[124:127], v[154:157], v[182:185], v[124:127]
	v_mfma_f32_16x16x32_bf16 v[120:123], v[146:149], v[190:193], v[120:123]
	v_mfma_f32_16x16x32_bf16 v[116:119], v[154:157], v[190:193], v[116:119]
	v_mfma_f32_16x16x32_bf16 v[104:107], v[146:149], v[198:201], v[104:107]
	v_mfma_f32_16x16x32_bf16 v[100:103], v[154:157], v[198:201], v[100:103]
	v_mfma_f32_16x16x32_bf16 v[88:91], v[146:149], v[206:209], v[88:91]
	v_mfma_f32_16x16x32_bf16 v[84:87], v[154:157], v[206:209], v[84:87]
	v_mfma_f32_16x16x32_bf16 v[128:131], v[150:153], v[186:189], v[128:131]
	v_mfma_f32_16x16x32_bf16 v[124:127], v[158:161], v[186:189], v[124:127]
	v_mfma_f32_16x16x32_bf16 v[120:123], v[150:153], v[194:197], v[120:123]
	v_mfma_f32_16x16x32_bf16 v[116:119], v[158:161], v[194:197], v[116:119]
	v_mfma_f32_16x16x32_bf16 v[104:107], v[150:153], v[202:205], v[104:107]
	v_mfma_f32_16x16x32_bf16 v[100:103], v[158:161], v[202:205], v[100:103]
	v_mfma_f32_16x16x32_bf16 v[88:91], v[150:153], v[226:229], v[88:91]
	v_mfma_f32_16x16x32_bf16 v[84:87], v[158:161], v[226:229], v[84:87]
	s_setprio 0
	s_setprio 1
	v_mfma_f32_16x16x32_bf16 v[112:115], v[162:165], v[182:185], v[112:115]
	v_mfma_f32_16x16x32_bf16 v[108:111], v[170:173], v[182:185], v[108:111]
	v_mfma_f32_16x16x32_bf16 v[96:99], v[162:165], v[190:193], v[96:99]
	v_mfma_f32_16x16x32_bf16 v[92:95], v[170:173], v[190:193], v[92:95]
	v_mfma_f32_16x16x32_bf16 v[80:83], v[162:165], v[198:201], v[80:83]
	v_mfma_f32_16x16x32_bf16 v[76:79], v[170:173], v[198:201], v[76:79]
	v_mfma_f32_16x16x32_bf16 v[72:75], v[162:165], v[206:209], v[72:75]
	v_mfma_f32_16x16x32_bf16 v[68:71], v[170:173], v[206:209], v[68:71]
	v_mfma_f32_16x16x32_bf16 v[112:115], v[166:169], v[186:189], v[112:115]
	v_mfma_f32_16x16x32_bf16 v[108:111], v[178:181], v[186:189], v[108:111]
	v_mfma_f32_16x16x32_bf16 v[96:99], v[166:169], v[194:197], v[96:99]
	v_mfma_f32_16x16x32_bf16 v[92:95], v[178:181], v[194:197], v[92:95]
	v_mfma_f32_16x16x32_bf16 v[80:83], v[166:169], v[202:205], v[80:83]
	v_mfma_f32_16x16x32_bf16 v[76:79], v[178:181], v[202:205], v[76:79]
	v_mfma_f32_16x16x32_bf16 v[72:75], v[166:169], v[226:229], v[72:75]
	v_mfma_f32_16x16x32_bf16 v[68:71], v[178:181], v[226:229], v[68:71]
	s_setprio 0
	s_barrier
	s_add_i32 s52, s68, s55
	v_lshl_add_u64 v[174:175], v[174:175], 0, s[6:7]
	s_mov_b32 m0, s52
	ds_read_b128 v[182:185], v145 offset:49152
	ds_read_b128 v[186:189], v145 offset:50176
	ds_read_b128 v[190:193], v145 offset:51200
	ds_read_b128 v[194:197], v145 offset:52224
	ds_read_b128 v[198:201], v145 offset:53248
	ds_read_b128 v[202:205], v145 offset:54272
	ds_read_b128 v[206:209], v145 offset:55296
	ds_read_b128 v[226:229], v145 offset:56320
	global_load_lds_dwordx4 v[174:175], off
	s_add_i32 m0, s52, 0x2000
	s_add_u32 s48, s48, 0x80080
	v_lshl_add_u64 v[174:175], v[210:211], 0, s[6:7]
	s_addc_u32 s49, s49, 0
	s_add_i32 s52, s69, s55
	global_load_lds_dwordx4 v[174:175], off
	v_lshl_add_u64 v[174:175], s[48:49], 0, v[2:3]
	s_mov_b32 m0, s52
	s_nop 0
	global_load_lds_dwordx4 v[174:175], off
	v_lshl_add_u64 v[174:175], s[48:49], 0, v[132:133]
	s_add_i32 m0, s52, 0x2000
	s_nop 0
	global_load_lds_dwordx4 v[174:175], off
	v_lshl_add_u64 v[174:175], v[214:215], 0, s[6:7]
	s_mov_b32 m0, s60
	s_nop 0
	global_load_lds_dwordx4 v[174:175], off
	v_lshl_add_u64 v[174:175], v[230:231], 0, s[6:7]
	s_mov_b32 m0, s61
	s_nop 0
	global_load_lds_dwordx4 v[174:175], off
	s_waitcnt vmcnt(8)
	s_waitcnt lgkmcnt(0)
	s_setprio 1
	s_barrier
	v_mfma_f32_16x16x32_bf16 v[64:67], v[146:149], v[182:185], v[64:67]
	v_mfma_f32_16x16x32_bf16 v[60:63], v[154:157], v[182:185], v[60:63]
	v_mfma_f32_16x16x32_bf16 v[56:59], v[146:149], v[190:193], v[56:59]
	v_mfma_f32_16x16x32_bf16 v[52:55], v[154:157], v[190:193], v[52:55]
	v_mfma_f32_16x16x32_bf16 v[40:43], v[146:149], v[198:201], v[40:43]
	v_mfma_f32_16x16x32_bf16 v[36:39], v[154:157], v[198:201], v[36:39]
	v_mfma_f32_16x16x32_bf16 v[24:27], v[146:149], v[206:209], v[24:27]
	v_mfma_f32_16x16x32_bf16 v[20:23], v[154:157], v[206:209], v[20:23]
	v_mfma_f32_16x16x32_bf16 v[64:67], v[150:153], v[186:189], v[64:67]
	v_mfma_f32_16x16x32_bf16 v[60:63], v[158:161], v[186:189], v[60:63]
	v_mfma_f32_16x16x32_bf16 v[56:59], v[150:153], v[194:197], v[56:59]
	v_mfma_f32_16x16x32_bf16 v[52:55], v[158:161], v[194:197], v[52:55]
	v_mfma_f32_16x16x32_bf16 v[40:43], v[150:153], v[202:205], v[40:43]
	v_mfma_f32_16x16x32_bf16 v[36:39], v[158:161], v[202:205], v[36:39]
	v_mfma_f32_16x16x32_bf16 v[24:27], v[150:153], v[226:229], v[24:27]
	v_mfma_f32_16x16x32_bf16 v[20:23], v[158:161], v[226:229], v[20:23]
	s_setprio 0
	s_setprio 1
	v_mfma_f32_16x16x32_bf16 v[48:51], v[162:165], v[182:185], v[48:51]
	v_mfma_f32_16x16x32_bf16 v[44:47], v[170:173], v[182:185], v[44:47]
	v_mfma_f32_16x16x32_bf16 v[32:35], v[162:165], v[190:193], v[32:35]
	v_mfma_f32_16x16x32_bf16 v[28:31], v[170:173], v[190:193], v[28:31]
	v_mfma_f32_16x16x32_bf16 v[16:19], v[162:165], v[198:201], v[16:19]
	v_mfma_f32_16x16x32_bf16 v[12:15], v[170:173], v[198:201], v[12:15]
	v_mfma_f32_16x16x32_bf16 v[8:11], v[162:165], v[206:209], v[8:11]
	v_mfma_f32_16x16x32_bf16 v[4:7], v[170:173], v[206:209], v[4:7]
	v_mfma_f32_16x16x32_bf16 v[48:51], v[166:169], v[186:189], v[48:51]
	v_mfma_f32_16x16x32_bf16 v[44:47], v[178:181], v[186:189], v[44:47]
	v_mfma_f32_16x16x32_bf16 v[32:35], v[166:169], v[194:197], v[32:35]
	v_mfma_f32_16x16x32_bf16 v[28:31], v[178:181], v[194:197], v[28:31]
	v_mfma_f32_16x16x32_bf16 v[16:19], v[166:169], v[202:205], v[16:19]
	v_mfma_f32_16x16x32_bf16 v[12:15], v[178:181], v[202:205], v[12:15]
	v_mfma_f32_16x16x32_bf16 v[8:11], v[166:169], v[226:229], v[8:11]
	v_mfma_f32_16x16x32_bf16 v[4:7], v[178:181], v[226:229], v[4:7]
	s_setprio 0
	s_barrier
	s_add_i32 s67, s67, 2
	s_add_u32 s46, s46, 0x100
	s_addc_u32 s47, s47, 0
	s_add_u32 s65, s65, 0x100
	s_addc_u32 s66, s66, 0
	s_cmp_gt_u32 s67, 29
	s_cbranch_scc0 .LBB0_398
	s_and_b64 vcc, exec, s[36:37]
	s_cbranch_vccz .LBB0_401
	s_barrier

.LBB0_585:
	s_add_u32 s42, s56, 0xfffe0080
	s_addc_u32 s43, s57, -1
	s_add_i32 s76, 0, 0x10000
	s_cmp_eq_u32 s75, 4
	s_cselect_b32 s61, s10, s43
	s_cselect_b32 s60, s11, s42
	s_cselect_b32 s59, s47, s74
	s_cselect_b32 s58, s49, s73
	s_add_i32 s77, 0, 0x14000
	ds_read_b128 v[146:149], v142
	ds_read_b128 v[150:153], v142 offset:1024
	ds_read_b128 v[154:157], v142 offset:2048
	ds_read_b128 v[158:161], v142 offset:3072
	ds_read_b128 v[162:165], v142 offset:16384
	ds_read_b128 v[166:169], v142 offset:17408
	ds_read_b128 v[170:173], v142 offset:18432
	ds_read_b128 v[178:181], v142 offset:19456
	v_lshl_add_u64 v[174:175], s[56:57], 0, v[138:139]
	s_add_i32 m0, s39, 0xc000
	ds_read_b128 v[182:185], v145
	ds_read_b128 v[186:189], v145 offset:1024
	ds_read_b128 v[190:193], v145 offset:2048
	ds_read_b128 v[194:197], v145 offset:3072
	ds_read_b128 v[198:201], v145 offset:4096
	ds_read_b128 v[202:205], v145 offset:5120
	ds_read_b128 v[206:209], v145 offset:6144
	ds_read_b128 v[226:229], v145 offset:7168
	global_load_lds_dwordx4 v[174:175], off
	v_lshl_add_u64 v[174:175], s[56:57], 0, v[140:141]
	s_add_i32 m0, s39, 0xe000
	s_nop 0
	global_load_lds_dwordx4 v[174:175], off
	s_waitcnt vmcnt(8)
	s_waitcnt lgkmcnt(0)
	s_setprio 1
	s_barrier
	v_mfma_f32_16x16x32_bf16 v[128:131], v[146:149], v[182:185], v[128:131]
	v_mfma_f32_16x16x32_bf16 v[124:127], v[154:157], v[182:185], v[124:127]
	v_mfma_f32_16x16x32_bf16 v[120:123], v[146:149], v[190:193], v[120:123]
	v_mfma_f32_16x16x32_bf16 v[116:119], v[154:157], v[190:193], v[116:119]
	v_mfma_f32_16x16x32_bf16 v[104:107], v[146:149], v[198:201], v[104:107]
	v_mfma_f32_16x16x32_bf16 v[100:103], v[154:157], v[198:201], v[100:103]
	v_mfma_f32_16x16x32_bf16 v[88:91], v[146:149], v[206:209], v[88:91]
	v_mfma_f32_16x16x32_bf16 v[84:87], v[154:157], v[206:209], v[84:87]
	v_mfma_f32_16x16x32_bf16 v[128:131], v[150:153], v[186:189], v[128:131]
	v_mfma_f32_16x16x32_bf16 v[124:127], v[158:161], v[186:189], v[124:127]
	v_mfma_f32_16x16x32_bf16 v[120:123], v[150:153], v[194:197], v[120:123]
	v_mfma_f32_16x16x32_bf16 v[116:119], v[158:161], v[194:197], v[116:119]
	v_mfma_f32_16x16x32_bf16 v[104:107], v[150:153], v[202:205], v[104:107]
	v_mfma_f32_16x16x32_bf16 v[100:103], v[158:161], v[202:205], v[100:103]
	v_mfma_f32_16x16x32_bf16 v[88:91], v[150:153], v[226:229], v[88:91]
	v_mfma_f32_16x16x32_bf16 v[84:87], v[158:161], v[226:229], v[84:87]
	s_setprio 0
	s_setprio 1
	v_mfma_f32_16x16x32_bf16 v[112:115], v[162:165], v[182:185], v[112:115]
	v_mfma_f32_16x16x32_bf16 v[108:111], v[170:173], v[182:185], v[108:111]
	v_mfma_f32_16x16x32_bf16 v[96:99], v[162:165], v[190:193], v[96:99]
	v_mfma_f32_16x16x32_bf16 v[92:95], v[170:173], v[190:193], v[92:95]
	v_mfma_f32_16x16x32_bf16 v[80:83], v[162:165], v[198:201], v[80:83]
	v_mfma_f32_16x16x32_bf16 v[76:79], v[170:173], v[198:201], v[76:79]
	v_mfma_f32_16x16x32_bf16 v[72:75], v[162:165], v[206:209], v[72:75]
	v_mfma_f32_16x16x32_bf16 v[68:71], v[170:173], v[206:209], v[68:71]
	v_mfma_f32_16x16x32_bf16 v[112:115], v[166:169], v[186:189], v[112:115]
	v_mfma_f32_16x16x32_bf16 v[108:111], v[178:181], v[186:189], v[108:111]
	v_mfma_f32_16x16x32_bf16 v[96:99], v[166:169], v[194:197], v[96:99]
	v_mfma_f32_16x16x32_bf16 v[92:95], v[178:181], v[194:197], v[92:95]
	v_mfma_f32_16x16x32_bf16 v[80:83], v[166:169], v[202:205], v[80:83]
	v_mfma_f32_16x16x32_bf16 v[76:79], v[178:181], v[202:205], v[76:79]
	v_mfma_f32_16x16x32_bf16 v[72:75], v[166:169], v[226:229], v[72:75]
	v_mfma_f32_16x16x32_bf16 v[68:71], v[178:181], v[226:229], v[68:71]
	s_setprio 0
	s_barrier
	s_add_i32 s42, s76, s67
	v_lshl_add_u64 v[174:175], s[58:59], 0, v[2:3]
	s_mov_b32 m0, s42
	ds_read_b128 v[182:185], v145 offset:16384
	ds_read_b128 v[186:189], v145 offset:17408
	ds_read_b128 v[190:193], v145 offset:18432
	ds_read_b128 v[194:197], v145 offset:19456
	ds_read_b128 v[198:201], v145 offset:20480
	ds_read_b128 v[202:205], v145 offset:21504
	ds_read_b128 v[206:209], v145 offset:22528
	ds_read_b128 v[226:229], v145 offset:23552
	global_load_lds_dwordx4 v[174:175], off
	s_add_i32 m0, s42, 0x2000
	s_add_u32 s42, s58, 0x20000
	v_lshl_add_u64 v[210:211], s[58:59], 0, v[132:133]
	s_addc_u32 s43, s59, 0
	s_add_i32 s76, s77, s67
	global_load_lds_dwordx4 v[210:211], off
	v_lshl_add_u64 v[214:215], s[42:43], 0, v[2:3]
	s_mov_b32 m0, s76
	v_lshl_add_u64 v[230:231], s[60:61], 0, v[134:135]
	global_load_lds_dwordx4 v[214:215], off
	v_lshl_add_u64 v[214:215], s[42:43], 0, v[132:133]
	s_add_i32 m0, s76, 0x2000
	s_nop 0
	global_load_lds_dwordx4 v[214:215], off
	v_lshl_add_u64 v[214:215], s[60:61], 0, v[136:137]
	s_mov_b32 m0, s39
	s_nop 0
	global_load_lds_dwordx4 v[214:215], off
	s_mov_b32 m0, s41
	s_nop 0
	global_load_lds_dwordx4 v[230:231], off
	s_waitcnt vmcnt(8)
	s_waitcnt lgkmcnt(0)
	s_setprio 1
	s_barrier
	v_mfma_f32_16x16x32_bf16 v[64:67], v[146:149], v[182:185], v[64:67]
	v_mfma_f32_16x16x32_bf16 v[60:63], v[154:157], v[182:185], v[60:63]
	v_mfma_f32_16x16x32_bf16 v[56:59], v[146:149], v[190:193], v[56:59]
	v_mfma_f32_16x16x32_bf16 v[52:55], v[154:157], v[190:193], v[52:55]
	v_mfma_f32_16x16x32_bf16 v[40:43], v[146:149], v[198:201], v[40:43]
	v_mfma_f32_16x16x32_bf16 v[36:39], v[154:157], v[198:201], v[36:39]
	v_mfma_f32_16x16x32_bf16 v[24:27], v[146:149], v[206:209], v[24:27]
	v_mfma_f32_16x16x32_bf16 v[20:23], v[154:157], v[206:209], v[20:23]
	v_mfma_f32_16x16x32_bf16 v[64:67], v[150:153], v[186:189], v[64:67]
	v_mfma_f32_16x16x32_bf16 v[60:63], v[158:161], v[186:189], v[60:63]
	v_mfma_f32_16x16x32_bf16 v[56:59], v[150:153], v[194:197], v[56:59]
	v_mfma_f32_16x16x32_bf16 v[52:55], v[158:161], v[194:197], v[52:55]
	v_mfma_f32_16x16x32_bf16 v[40:43], v[150:153], v[202:205], v[40:43]
	v_mfma_f32_16x16x32_bf16 v[36:39], v[158:161], v[202:205], v[36:39]
	v_mfma_f32_16x16x32_bf16 v[24:27], v[150:153], v[226:229], v[24:27]
	v_mfma_f32_16x16x32_bf16 v[20:23], v[158:161], v[226:229], v[20:23]
	s_setprio 0
	s_setprio 1
	v_mfma_f32_16x16x32_bf16 v[48:51], v[162:165], v[182:185], v[48:51]
	v_mfma_f32_16x16x32_bf16 v[44:47], v[170:173], v[182:185], v[44:47]
	v_mfma_f32_16x16x32_bf16 v[32:35], v[162:165], v[190:193], v[32:35]
	v_mfma_f32_16x16x32_bf16 v[28:31], v[170:173], v[190:193], v[28:31]
	v_mfma_f32_16x16x32_bf16 v[16:19], v[162:165], v[198:201], v[16:19]
	v_mfma_f32_16x16x32_bf16 v[12:15], v[170:173], v[198:201], v[12:15]
	v_mfma_f32_16x16x32_bf16 v[8:11], v[162:165], v[206:209], v[8:11]
	v_mfma_f32_16x16x32_bf16 v[4:7], v[170:173], v[206:209], v[4:7]
	v_mfma_f32_16x16x32_bf16 v[48:51], v[166:169], v[186:189], v[48:51]
	v_mfma_f32_16x16x32_bf16 v[44:47], v[178:181], v[186:189], v[44:47]
	v_mfma_f32_16x16x32_bf16 v[32:35], v[166:169], v[194:197], v[32:35]
	v_mfma_f32_16x16x32_bf16 v[28:31], v[178:181], v[194:197], v[28:31]
	v_mfma_f32_16x16x32_bf16 v[16:19], v[166:169], v[202:205], v[16:19]
	v_mfma_f32_16x16x32_bf16 v[12:15], v[178:181], v[202:205], v[12:15]
	v_mfma_f32_16x16x32_bf16 v[8:11], v[166:169], v[226:229], v[8:11]
	v_mfma_f32_16x16x32_bf16 v[4:7], v[178:181], v[226:229], v[4:7]
	s_setprio 0
	s_barrier
	s_add_i32 s76, 0, 0x18000
	s_add_i32 s77, 0, 0x1c000
	ds_read_b128 v[146:149], v142 offset:32768
	ds_read_b128 v[150:153], v142 offset:33792
	ds_read_b128 v[154:157], v142 offset:34816
	ds_read_b128 v[158:161], v142 offset:35840
	ds_read_b128 v[162:165], v142 offset:49152
	ds_read_b128 v[166:169], v142 offset:50176
	ds_read_b128 v[170:173], v142 offset:51200
	ds_read_b128 v[178:181], v142 offset:52224
	s_add_u32 s42, s60, 0x20000
	s_addc_u32 s43, s61, 0
	s_mov_b32 m0, s68
	v_lshl_add_u64 v[232:233], s[42:43], 0, v[136:137]
	ds_read_b128 v[182:185], v145 offset:32768
	ds_read_b128 v[186:189], v145 offset:33792
	ds_read_b128 v[190:193], v145 offset:34816
	ds_read_b128 v[194:197], v145 offset:35840
	ds_read_b128 v[198:201], v145 offset:36864
	ds_read_b128 v[202:205], v145 offset:37888
	ds_read_b128 v[206:209], v145 offset:38912
	ds_read_b128 v[226:229], v145 offset:39936
	global_load_lds_dwordx4 v[232:233], off
	v_lshl_add_u64 v[232:233], s[42:43], 0, v[134:135]
	s_mov_b32 m0, s69
	s_nop 0
	global_load_lds_dwordx4 v[232:233], off
	s_waitcnt vmcnt(8)
	s_waitcnt lgkmcnt(0)
	s_setprio 1
	s_barrier
	v_mfma_f32_16x16x32_bf16 v[128:131], v[146:149], v[182:185], v[128:131]
	v_mfma_f32_16x16x32_bf16 v[124:127], v[154:157], v[182:185], v[124:127]
	v_mfma_f32_16x16x32_bf16 v[120:123], v[146:149], v[190:193], v[120:123]
	v_mfma_f32_16x16x32_bf16 v[116:119], v[154:157], v[190:193], v[116:119]
	v_mfma_f32_16x16x32_bf16 v[104:107], v[146:149], v[198:201], v[104:107]
	v_mfma_f32_16x16x32_bf16 v[100:103], v[154:157], v[198:201], v[100:103]
	v_mfma_f32_16x16x32_bf16 v[88:91], v[146:149], v[206:209], v[88:91]
	v_mfma_f32_16x16x32_bf16 v[84:87], v[154:157], v[206:209], v[84:87]
	v_mfma_f32_16x16x32_bf16 v[128:131], v[150:153], v[186:189], v[128:131]
	v_mfma_f32_16x16x32_bf16 v[124:127], v[158:161], v[186:189], v[124:127]
	v_mfma_f32_16x16x32_bf16 v[120:123], v[150:153], v[194:197], v[120:123]
	v_mfma_f32_16x16x32_bf16 v[116:119], v[158:161], v[194:197], v[116:119]
	v_mfma_f32_16x16x32_bf16 v[104:107], v[150:153], v[202:205], v[104:107]
	v_mfma_f32_16x16x32_bf16 v[100:103], v[158:161], v[202:205], v[100:103]
	v_mfma_f32_16x16x32_bf16 v[88:91], v[150:153], v[226:229], v[88:91]
	v_mfma_f32_16x16x32_bf16 v[84:87], v[158:161], v[226:229], v[84:87]
	s_setprio 0
	s_setprio 1
	v_mfma_f32_16x16x32_bf16 v[112:115], v[162:165], v[182:185], v[112:115]
	v_mfma_f32_16x16x32_bf16 v[108:111], v[170:173], v[182:185], v[108:111]
	v_mfma_f32_16x16x32_bf16 v[96:99], v[162:165], v[190:193], v[96:99]
	v_mfma_f32_16x16x32_bf16 v[92:95], v[170:173], v[190:193], v[92:95]
	v_mfma_f32_16x16x32_bf16 v[80:83], v[162:165], v[198:201], v[80:83]
	v_mfma_f32_16x16x32_bf16 v[76:79], v[170:173], v[198:201], v[76:79]
	v_mfma_f32_16x16x32_bf16 v[72:75], v[162:165], v[206:209], v[72:75]
	v_mfma_f32_16x16x32_bf16 v[68:71], v[170:173], v[206:209], v[68:71]
	v_mfma_f32_16x16x32_bf16 v[112:115], v[166:169], v[186:189], v[112:115]
	v_mfma_f32_16x16x32_bf16 v[108:111], v[178:181], v[186:189], v[108:111]
	v_mfma_f32_16x16x32_bf16 v[96:99], v[166:169], v[194:197], v[96:99]
	v_mfma_f32_16x16x32_bf16 v[92:95], v[178:181], v[194:197], v[92:95]
	v_mfma_f32_16x16x32_bf16 v[80:83], v[166:169], v[202:205], v[80:83]
	v_mfma_f32_16x16x32_bf16 v[76:79], v[178:181], v[202:205], v[76:79]
	v_mfma_f32_16x16x32_bf16 v[72:75], v[166:169], v[226:229], v[72:75]
	v_mfma_f32_16x16x32_bf16 v[68:71], v[178:181], v[226:229], v[68:71]
	s_setprio 0
	s_barrier
	s_add_i32 s42, s76, s67
	v_lshl_add_u64 v[174:175], v[174:175], 0, s[6:7]
	s_mov_b32 m0, s42
	ds_read_b128 v[182:185], v145 offset:49152
	ds_read_b128 v[186:189], v145 offset:50176
	ds_read_b128 v[190:193], v145 offset:51200
	ds_read_b128 v[194:197], v145 offset:52224
	ds_read_b128 v[198:201], v145 offset:53248
	ds_read_b128 v[202:205], v145 offset:54272
	ds_read_b128 v[206:209], v145 offset:55296
	ds_read_b128 v[226:229], v145 offset:56320
	global_load_lds_dwordx4 v[174:175], off
	s_add_i32 m0, s42, 0x2000
	s_add_u32 s42, s58, 0x20080
	v_lshl_add_u64 v[174:175], v[210:211], 0, s[6:7]
	s_addc_u32 s43, s59, 0
	s_add_i32 s58, s77, s67
	global_load_lds_dwordx4 v[174:175], off
	v_lshl_add_u64 v[174:175], s[42:43], 0, v[2:3]
	s_mov_b32 m0, s58
	s_nop 0
	global_load_lds_dwordx4 v[174:175], off
	v_lshl_add_u64 v[174:175], s[42:43], 0, v[132:133]
	s_add_i32 m0, s58, 0x2000
	s_nop 0
	global_load_lds_dwordx4 v[174:175], off
	v_lshl_add_u64 v[174:175], v[214:215], 0, s[6:7]
	s_mov_b32 m0, s70
	s_nop 0
	global_load_lds_dwordx4 v[174:175], off
	v_lshl_add_u64 v[174:175], v[230:231], 0, s[6:7]
	s_mov_b32 m0, s71
	s_nop 0
	global_load_lds_dwordx4 v[174:175], off
	s_waitcnt vmcnt(8)
	s_waitcnt lgkmcnt(0)
	s_setprio 1
	s_barrier
	v_mfma_f32_16x16x32_bf16 v[64:67], v[146:149], v[182:185], v[64:67]
	v_mfma_f32_16x16x32_bf16 v[60:63], v[154:157], v[182:185], v[60:63]
	v_mfma_f32_16x16x32_bf16 v[56:59], v[146:149], v[190:193], v[56:59]
	v_mfma_f32_16x16x32_bf16 v[52:55], v[154:157], v[190:193], v[52:55]
	v_mfma_f32_16x16x32_bf16 v[40:43], v[146:149], v[198:201], v[40:43]
	v_mfma_f32_16x16x32_bf16 v[36:39], v[154:157], v[198:201], v[36:39]
	v_mfma_f32_16x16x32_bf16 v[24:27], v[146:149], v[206:209], v[24:27]
	v_mfma_f32_16x16x32_bf16 v[20:23], v[154:157], v[206:209], v[20:23]
	v_mfma_f32_16x16x32_bf16 v[64:67], v[150:153], v[186:189], v[64:67]
	v_mfma_f32_16x16x32_bf16 v[60:63], v[158:161], v[186:189], v[60:63]
	v_mfma_f32_16x16x32_bf16 v[56:59], v[150:153], v[194:197], v[56:59]
	v_mfma_f32_16x16x32_bf16 v[52:55], v[158:161], v[194:197], v[52:55]
	v_mfma_f32_16x16x32_bf16 v[40:43], v[150:153], v[202:205], v[40:43]
	v_mfma_f32_16x16x32_bf16 v[36:39], v[158:161], v[202:205], v[36:39]
	v_mfma_f32_16x16x32_bf16 v[24:27], v[150:153], v[226:229], v[24:27]
	v_mfma_f32_16x16x32_bf16 v[20:23], v[158:161], v[226:229], v[20:23]
	s_setprio 0
	s_setprio 1
	v_mfma_f32_16x16x32_bf16 v[48:51], v[162:165], v[182:185], v[48:51]
	v_mfma_f32_16x16x32_bf16 v[44:47], v[170:173], v[182:185], v[44:47]
	v_mfma_f32_16x16x32_bf16 v[32:35], v[162:165], v[190:193], v[32:35]
	v_mfma_f32_16x16x32_bf16 v[28:31], v[170:173], v[190:193], v[28:31]
	v_mfma_f32_16x16x32_bf16 v[16:19], v[162:165], v[198:201], v[16:19]
	v_mfma_f32_16x16x32_bf16 v[12:15], v[170:173], v[198:201], v[12:15]
	v_mfma_f32_16x16x32_bf16 v[8:11], v[162:165], v[206:209], v[8:11]
	v_mfma_f32_16x16x32_bf16 v[4:7], v[170:173], v[206:209], v[4:7]
	v_mfma_f32_16x16x32_bf16 v[48:51], v[166:169], v[186:189], v[48:51]
	v_mfma_f32_16x16x32_bf16 v[44:47], v[178:181], v[186:189], v[44:47]
	v_mfma_f32_16x16x32_bf16 v[32:35], v[166:169], v[194:197], v[32:35]
	v_mfma_f32_16x16x32_bf16 v[28:31], v[178:181], v[194:197], v[28:31]
	v_mfma_f32_16x16x32_bf16 v[16:19], v[166:169], v[202:205], v[16:19]
	v_mfma_f32_16x16x32_bf16 v[12:15], v[178:181], v[202:205], v[12:15]
	v_mfma_f32_16x16x32_bf16 v[8:11], v[166:169], v[226:229], v[8:11]
	v_mfma_f32_16x16x32_bf16 v[4:7], v[178:181], v[226:229], v[4:7]
	s_setprio 0
	s_barrier
	s_add_i32 s75, s75, 2
	s_add_u32 s56, s56, 0x100
	s_addc_u32 s57, s57, 0
	s_add_u32 s73, s73, 0x100
	s_addc_u32 s74, s74, 0
	s_cmp_gt_u32 s75, 5
	s_cbranch_scc0 .LBB0_585
	s_and_b64 vcc, exec, s[44:45]
	s_cbranch_vccz .LBB0_588
	s_barrier

.LBB0_1427:
	s_add_u32 s42, s48, 0xfff80080
	s_addc_u32 s43, s49, -1
	s_add_i32 s70, 0, 0x10000
	s_cmp_eq_u32 s69, 28
	s_cselect_b32 s55, s10, s43
	s_cselect_b32 s54, s11, s42
	s_cselect_b32 s53, s39, s68
	s_cselect_b32 s52, s41, s67
	s_add_i32 s71, 0, 0x14000
	ds_read_b128 v[146:149], v142
	ds_read_b128 v[150:153], v142 offset:1024
	ds_read_b128 v[154:157], v142 offset:2048
	ds_read_b128 v[158:161], v142 offset:3072
	ds_read_b128 v[162:165], v142 offset:16384
	ds_read_b128 v[166:169], v142 offset:17408
	ds_read_b128 v[170:173], v142 offset:18432
	ds_read_b128 v[178:181], v142 offset:19456
	v_lshl_add_u64 v[174:175], s[48:49], 0, v[138:139]
	s_add_i32 m0, s58, 0xc000
	ds_read_b128 v[182:185], v145
	ds_read_b128 v[186:189], v145 offset:1024
	ds_read_b128 v[190:193], v145 offset:2048
	ds_read_b128 v[194:197], v145 offset:3072
	ds_read_b128 v[198:201], v145 offset:4096
	ds_read_b128 v[202:205], v145 offset:5120
	ds_read_b128 v[206:209], v145 offset:6144
	ds_read_b128 v[226:229], v145 offset:7168
	global_load_lds_dwordx4 v[174:175], off
	v_lshl_add_u64 v[174:175], s[48:49], 0, v[140:141]
	s_add_i32 m0, s58, 0xe000
	s_nop 0
	global_load_lds_dwordx4 v[174:175], off
	s_waitcnt vmcnt(8)
	s_waitcnt lgkmcnt(0)
	s_setprio 1
	s_barrier
	v_mfma_f32_16x16x32_bf16 v[128:131], v[146:149], v[182:185], v[128:131]
	v_mfma_f32_16x16x32_bf16 v[124:127], v[154:157], v[182:185], v[124:127]
	v_mfma_f32_16x16x32_bf16 v[120:123], v[146:149], v[190:193], v[120:123]
	v_mfma_f32_16x16x32_bf16 v[116:119], v[154:157], v[190:193], v[116:119]
	v_mfma_f32_16x16x32_bf16 v[104:107], v[146:149], v[198:201], v[104:107]
	v_mfma_f32_16x16x32_bf16 v[100:103], v[154:157], v[198:201], v[100:103]
	v_mfma_f32_16x16x32_bf16 v[88:91], v[146:149], v[206:209], v[88:91]
	v_mfma_f32_16x16x32_bf16 v[84:87], v[154:157], v[206:209], v[84:87]
	v_mfma_f32_16x16x32_bf16 v[128:131], v[150:153], v[186:189], v[128:131]
	v_mfma_f32_16x16x32_bf16 v[124:127], v[158:161], v[186:189], v[124:127]
	v_mfma_f32_16x16x32_bf16 v[120:123], v[150:153], v[194:197], v[120:123]
	v_mfma_f32_16x16x32_bf16 v[116:119], v[158:161], v[194:197], v[116:119]
	v_mfma_f32_16x16x32_bf16 v[104:107], v[150:153], v[202:205], v[104:107]
	v_mfma_f32_16x16x32_bf16 v[100:103], v[158:161], v[202:205], v[100:103]
	v_mfma_f32_16x16x32_bf16 v[88:91], v[150:153], v[226:229], v[88:91]
	v_mfma_f32_16x16x32_bf16 v[84:87], v[158:161], v[226:229], v[84:87]
	s_setprio 0
	s_setprio 1
	v_mfma_f32_16x16x32_bf16 v[112:115], v[162:165], v[182:185], v[112:115]
	v_mfma_f32_16x16x32_bf16 v[108:111], v[170:173], v[182:185], v[108:111]
	v_mfma_f32_16x16x32_bf16 v[96:99], v[162:165], v[190:193], v[96:99]
	v_mfma_f32_16x16x32_bf16 v[92:95], v[170:173], v[190:193], v[92:95]
	v_mfma_f32_16x16x32_bf16 v[80:83], v[162:165], v[198:201], v[80:83]
	v_mfma_f32_16x16x32_bf16 v[76:79], v[170:173], v[198:201], v[76:79]
	v_mfma_f32_16x16x32_bf16 v[72:75], v[162:165], v[206:209], v[72:75]
	v_mfma_f32_16x16x32_bf16 v[68:71], v[170:173], v[206:209], v[68:71]
	v_mfma_f32_16x16x32_bf16 v[112:115], v[166:169], v[186:189], v[112:115]
	v_mfma_f32_16x16x32_bf16 v[108:111], v[178:181], v[186:189], v[108:111]
	v_mfma_f32_16x16x32_bf16 v[96:99], v[166:169], v[194:197], v[96:99]
	v_mfma_f32_16x16x32_bf16 v[92:95], v[178:181], v[194:197], v[92:95]
	v_mfma_f32_16x16x32_bf16 v[80:83], v[166:169], v[202:205], v[80:83]
	v_mfma_f32_16x16x32_bf16 v[76:79], v[178:181], v[202:205], v[76:79]
	v_mfma_f32_16x16x32_bf16 v[72:75], v[166:169], v[226:229], v[72:75]
	v_mfma_f32_16x16x32_bf16 v[68:71], v[178:181], v[226:229], v[68:71]
	s_setprio 0
	s_barrier
	s_add_i32 s42, s70, s57
	v_lshl_add_u64 v[174:175], s[52:53], 0, v[2:3]
	s_mov_b32 m0, s42
	ds_read_b128 v[182:185], v145 offset:16384
	ds_read_b128 v[186:189], v145 offset:17408
	ds_read_b128 v[190:193], v145 offset:18432
	ds_read_b128 v[194:197], v145 offset:19456
	ds_read_b128 v[198:201], v145 offset:20480
	ds_read_b128 v[202:205], v145 offset:21504
	ds_read_b128 v[206:209], v145 offset:22528
	ds_read_b128 v[226:229], v145 offset:23552
	global_load_lds_dwordx4 v[174:175], off
	s_add_i32 m0, s42, 0x2000
	s_add_u32 s42, s52, 0x80000
	v_lshl_add_u64 v[210:211], s[52:53], 0, v[132:133]
	s_addc_u32 s43, s53, 0
	s_add_i32 s70, s71, s57
	global_load_lds_dwordx4 v[210:211], off
	v_lshl_add_u64 v[214:215], s[42:43], 0, v[2:3]
	s_mov_b32 m0, s70
	v_lshl_add_u64 v[230:231], s[54:55], 0, v[134:135]
	global_load_lds_dwordx4 v[214:215], off
	v_lshl_add_u64 v[214:215], s[42:43], 0, v[132:133]
	s_add_i32 m0, s70, 0x2000
	s_nop 0
	global_load_lds_dwordx4 v[214:215], off
	v_lshl_add_u64 v[214:215], s[54:55], 0, v[136:137]
	s_mov_b32 m0, s58
	s_nop 0
	global_load_lds_dwordx4 v[214:215], off
	s_mov_b32 m0, s59
	s_nop 0
	global_load_lds_dwordx4 v[230:231], off
	s_waitcnt vmcnt(8)
	s_waitcnt lgkmcnt(0)
	s_setprio 1
	s_barrier
	v_mfma_f32_16x16x32_bf16 v[64:67], v[146:149], v[182:185], v[64:67]
	v_mfma_f32_16x16x32_bf16 v[60:63], v[154:157], v[182:185], v[60:63]
	v_mfma_f32_16x16x32_bf16 v[56:59], v[146:149], v[190:193], v[56:59]
	v_mfma_f32_16x16x32_bf16 v[52:55], v[154:157], v[190:193], v[52:55]
	v_mfma_f32_16x16x32_bf16 v[40:43], v[146:149], v[198:201], v[40:43]
	v_mfma_f32_16x16x32_bf16 v[36:39], v[154:157], v[198:201], v[36:39]
	v_mfma_f32_16x16x32_bf16 v[24:27], v[146:149], v[206:209], v[24:27]
	v_mfma_f32_16x16x32_bf16 v[20:23], v[154:157], v[206:209], v[20:23]
	v_mfma_f32_16x16x32_bf16 v[64:67], v[150:153], v[186:189], v[64:67]
	v_mfma_f32_16x16x32_bf16 v[60:63], v[158:161], v[186:189], v[60:63]
	v_mfma_f32_16x16x32_bf16 v[56:59], v[150:153], v[194:197], v[56:59]
	v_mfma_f32_16x16x32_bf16 v[52:55], v[158:161], v[194:197], v[52:55]
	v_mfma_f32_16x16x32_bf16 v[40:43], v[150:153], v[202:205], v[40:43]
	v_mfma_f32_16x16x32_bf16 v[36:39], v[158:161], v[202:205], v[36:39]
	v_mfma_f32_16x16x32_bf16 v[24:27], v[150:153], v[226:229], v[24:27]
	v_mfma_f32_16x16x32_bf16 v[20:23], v[158:161], v[226:229], v[20:23]
	s_setprio 0
	s_setprio 1
	v_mfma_f32_16x16x32_bf16 v[48:51], v[162:165], v[182:185], v[48:51]
	v_mfma_f32_16x16x32_bf16 v[44:47], v[170:173], v[182:185], v[44:47]
	v_mfma_f32_16x16x32_bf16 v[32:35], v[162:165], v[190:193], v[32:35]
	v_mfma_f32_16x16x32_bf16 v[28:31], v[170:173], v[190:193], v[28:31]
	v_mfma_f32_16x16x32_bf16 v[16:19], v[162:165], v[198:201], v[16:19]
	v_mfma_f32_16x16x32_bf16 v[12:15], v[170:173], v[198:201], v[12:15]
	v_mfma_f32_16x16x32_bf16 v[8:11], v[162:165], v[206:209], v[8:11]
	v_mfma_f32_16x16x32_bf16 v[4:7], v[170:173], v[206:209], v[4:7]
	v_mfma_f32_16x16x32_bf16 v[48:51], v[166:169], v[186:189], v[48:51]
	v_mfma_f32_16x16x32_bf16 v[44:47], v[178:181], v[186:189], v[44:47]
	v_mfma_f32_16x16x32_bf16 v[32:35], v[166:169], v[194:197], v[32:35]
	v_mfma_f32_16x16x32_bf16 v[28:31], v[178:181], v[194:197], v[28:31]
	v_mfma_f32_16x16x32_bf16 v[16:19], v[166:169], v[202:205], v[16:19]
	v_mfma_f32_16x16x32_bf16 v[12:15], v[178:181], v[202:205], v[12:15]
	v_mfma_f32_16x16x32_bf16 v[8:11], v[166:169], v[226:229], v[8:11]
	v_mfma_f32_16x16x32_bf16 v[4:7], v[178:181], v[226:229], v[4:7]
	s_setprio 0
	s_barrier
	s_add_i32 s70, 0, 0x18000
	s_add_i32 s71, 0, 0x1c000
	ds_read_b128 v[146:149], v142 offset:32768
	ds_read_b128 v[150:153], v142 offset:33792
	ds_read_b128 v[154:157], v142 offset:34816
	ds_read_b128 v[158:161], v142 offset:35840
	ds_read_b128 v[162:165], v142 offset:49152
	ds_read_b128 v[166:169], v142 offset:50176
	ds_read_b128 v[170:173], v142 offset:51200
	ds_read_b128 v[178:181], v142 offset:52224
	s_add_u32 s42, s54, 0x80000
	s_addc_u32 s43, s55, 0
	s_mov_b32 m0, s60
	v_lshl_add_u64 v[232:233], s[42:43], 0, v[136:137]
	ds_read_b128 v[182:185], v145 offset:32768
	ds_read_b128 v[186:189], v145 offset:33792
	ds_read_b128 v[190:193], v145 offset:34816
	ds_read_b128 v[194:197], v145 offset:35840
	ds_read_b128 v[198:201], v145 offset:36864
	ds_read_b128 v[202:205], v145 offset:37888
	ds_read_b128 v[206:209], v145 offset:38912
	ds_read_b128 v[226:229], v145 offset:39936
	global_load_lds_dwordx4 v[232:233], off
	v_lshl_add_u64 v[232:233], s[42:43], 0, v[134:135]
	s_mov_b32 m0, s61
	s_nop 0
	global_load_lds_dwordx4 v[232:233], off
	s_waitcnt vmcnt(8)
	s_waitcnt lgkmcnt(0)
	s_setprio 1
	s_barrier
	v_mfma_f32_16x16x32_bf16 v[128:131], v[146:149], v[182:185], v[128:131]
	v_mfma_f32_16x16x32_bf16 v[124:127], v[154:157], v[182:185], v[124:127]
	v_mfma_f32_16x16x32_bf16 v[120:123], v[146:149], v[190:193], v[120:123]
	v_mfma_f32_16x16x32_bf16 v[116:119], v[154:157], v[190:193], v[116:119]
	v_mfma_f32_16x16x32_bf16 v[104:107], v[146:149], v[198:201], v[104:107]
	v_mfma_f32_16x16x32_bf16 v[100:103], v[154:157], v[198:201], v[100:103]
	v_mfma_f32_16x16x32_bf16 v[88:91], v[146:149], v[206:209], v[88:91]
	v_mfma_f32_16x16x32_bf16 v[84:87], v[154:157], v[206:209], v[84:87]
	v_mfma_f32_16x16x32_bf16 v[128:131], v[150:153], v[186:189], v[128:131]
	v_mfma_f32_16x16x32_bf16 v[124:127], v[158:161], v[186:189], v[124:127]
	v_mfma_f32_16x16x32_bf16 v[120:123], v[150:153], v[194:197], v[120:123]
	v_mfma_f32_16x16x32_bf16 v[116:119], v[158:161], v[194:197], v[116:119]
	v_mfma_f32_16x16x32_bf16 v[104:107], v[150:153], v[202:205], v[104:107]
	v_mfma_f32_16x16x32_bf16 v[100:103], v[158:161], v[202:205], v[100:103]
	v_mfma_f32_16x16x32_bf16 v[88:91], v[150:153], v[226:229], v[88:91]
	v_mfma_f32_16x16x32_bf16 v[84:87], v[158:161], v[226:229], v[84:87]
	s_setprio 0
	s_setprio 1
	v_mfma_f32_16x16x32_bf16 v[112:115], v[162:165], v[182:185], v[112:115]
	v_mfma_f32_16x16x32_bf16 v[108:111], v[170:173], v[182:185], v[108:111]
	v_mfma_f32_16x16x32_bf16 v[96:99], v[162:165], v[190:193], v[96:99]
	v_mfma_f32_16x16x32_bf16 v[92:95], v[170:173], v[190:193], v[92:95]
	v_mfma_f32_16x16x32_bf16 v[80:83], v[162:165], v[198:201], v[80:83]
	v_mfma_f32_16x16x32_bf16 v[76:79], v[170:173], v[198:201], v[76:79]
	v_mfma_f32_16x16x32_bf16 v[72:75], v[162:165], v[206:209], v[72:75]
	v_mfma_f32_16x16x32_bf16 v[68:71], v[170:173], v[206:209], v[68:71]
	v_mfma_f32_16x16x32_bf16 v[112:115], v[166:169], v[186:189], v[112:115]
	v_mfma_f32_16x16x32_bf16 v[108:111], v[178:181], v[186:189], v[108:111]
	v_mfma_f32_16x16x32_bf16 v[96:99], v[166:169], v[194:197], v[96:99]
	v_mfma_f32_16x16x32_bf16 v[92:95], v[178:181], v[194:197], v[92:95]
	v_mfma_f32_16x16x32_bf16 v[80:83], v[166:169], v[202:205], v[80:83]
	v_mfma_f32_16x16x32_bf16 v[76:79], v[178:181], v[202:205], v[76:79]
	v_mfma_f32_16x16x32_bf16 v[72:75], v[166:169], v[226:229], v[72:75]
	v_mfma_f32_16x16x32_bf16 v[68:71], v[178:181], v[226:229], v[68:71]
	s_setprio 0
	s_barrier
	s_add_i32 s42, s70, s57
	v_lshl_add_u64 v[174:175], v[174:175], 0, s[6:7]
	s_mov_b32 m0, s42
	ds_read_b128 v[182:185], v145 offset:49152
	ds_read_b128 v[186:189], v145 offset:50176
	ds_read_b128 v[190:193], v145 offset:51200
	ds_read_b128 v[194:197], v145 offset:52224
	ds_read_b128 v[198:201], v145 offset:53248
	ds_read_b128 v[202:205], v145 offset:54272
	ds_read_b128 v[206:209], v145 offset:55296
	ds_read_b128 v[226:229], v145 offset:56320
	global_load_lds_dwordx4 v[174:175], off
	s_add_i32 m0, s42, 0x2000
	s_add_u32 s42, s52, 0x80080
	v_lshl_add_u64 v[174:175], v[210:211], 0, s[6:7]
	s_addc_u32 s43, s53, 0
	s_add_i32 s52, s71, s57
	global_load_lds_dwordx4 v[174:175], off
	v_lshl_add_u64 v[174:175], s[42:43], 0, v[2:3]
	s_mov_b32 m0, s52
	s_nop 0
	global_load_lds_dwordx4 v[174:175], off
	v_lshl_add_u64 v[174:175], s[42:43], 0, v[132:133]
	s_add_i32 m0, s52, 0x2000
	s_nop 0
	global_load_lds_dwordx4 v[174:175], off
	v_lshl_add_u64 v[174:175], v[214:215], 0, s[6:7]
	s_mov_b32 m0, s62
	s_nop 0
	global_load_lds_dwordx4 v[174:175], off
	v_lshl_add_u64 v[174:175], v[230:231], 0, s[6:7]
	s_mov_b32 m0, s63
	s_nop 0
	global_load_lds_dwordx4 v[174:175], off
	s_waitcnt vmcnt(8)
	s_waitcnt lgkmcnt(0)
	s_setprio 1
	s_barrier
	v_mfma_f32_16x16x32_bf16 v[64:67], v[146:149], v[182:185], v[64:67]
	v_mfma_f32_16x16x32_bf16 v[60:63], v[154:157], v[182:185], v[60:63]
	v_mfma_f32_16x16x32_bf16 v[56:59], v[146:149], v[190:193], v[56:59]
	v_mfma_f32_16x16x32_bf16 v[52:55], v[154:157], v[190:193], v[52:55]
	v_mfma_f32_16x16x32_bf16 v[40:43], v[146:149], v[198:201], v[40:43]
	v_mfma_f32_16x16x32_bf16 v[36:39], v[154:157], v[198:201], v[36:39]
	v_mfma_f32_16x16x32_bf16 v[24:27], v[146:149], v[206:209], v[24:27]
	v_mfma_f32_16x16x32_bf16 v[20:23], v[154:157], v[206:209], v[20:23]
	v_mfma_f32_16x16x32_bf16 v[64:67], v[150:153], v[186:189], v[64:67]
	v_mfma_f32_16x16x32_bf16 v[60:63], v[158:161], v[186:189], v[60:63]
	v_mfma_f32_16x16x32_bf16 v[56:59], v[150:153], v[194:197], v[56:59]
	v_mfma_f32_16x16x32_bf16 v[52:55], v[158:161], v[194:197], v[52:55]
	v_mfma_f32_16x16x32_bf16 v[40:43], v[150:153], v[202:205], v[40:43]
	v_mfma_f32_16x16x32_bf16 v[36:39], v[158:161], v[202:205], v[36:39]
	v_mfma_f32_16x16x32_bf16 v[24:27], v[150:153], v[226:229], v[24:27]
	v_mfma_f32_16x16x32_bf16 v[20:23], v[158:161], v[226:229], v[20:23]
	s_setprio 0
	s_setprio 1
	v_mfma_f32_16x16x32_bf16 v[48:51], v[162:165], v[182:185], v[48:51]
	v_mfma_f32_16x16x32_bf16 v[44:47], v[170:173], v[182:185], v[44:47]
	v_mfma_f32_16x16x32_bf16 v[32:35], v[162:165], v[190:193], v[32:35]
	v_mfma_f32_16x16x32_bf16 v[28:31], v[170:173], v[190:193], v[28:31]
	v_mfma_f32_16x16x32_bf16 v[16:19], v[162:165], v[198:201], v[16:19]
	v_mfma_f32_16x16x32_bf16 v[12:15], v[170:173], v[198:201], v[12:15]
	v_mfma_f32_16x16x32_bf16 v[8:11], v[162:165], v[206:209], v[8:11]
	v_mfma_f32_16x16x32_bf16 v[4:7], v[170:173], v[206:209], v[4:7]
	v_mfma_f32_16x16x32_bf16 v[48:51], v[166:169], v[186:189], v[48:51]
	v_mfma_f32_16x16x32_bf16 v[44:47], v[178:181], v[186:189], v[44:47]
	v_mfma_f32_16x16x32_bf16 v[32:35], v[166:169], v[194:197], v[32:35]
	v_mfma_f32_16x16x32_bf16 v[28:31], v[178:181], v[194:197], v[28:31]
	v_mfma_f32_16x16x32_bf16 v[16:19], v[166:169], v[202:205], v[16:19]
	v_mfma_f32_16x16x32_bf16 v[12:15], v[178:181], v[202:205], v[12:15]
	v_mfma_f32_16x16x32_bf16 v[8:11], v[166:169], v[226:229], v[8:11]
	v_mfma_f32_16x16x32_bf16 v[4:7], v[178:181], v[226:229], v[4:7]
	s_setprio 0
	s_barrier
	s_add_i32 s69, s69, 2
	s_add_u32 s48, s48, 0x100
	s_addc_u32 s49, s49, 0
	s_add_u32 s67, s67, 0x100
	s_addc_u32 s68, s68, 0
	s_cmp_gt_u32 s69, 29
	s_cbranch_scc0 .LBB0_1427
	s_and_b64 vcc, exec, s[36:37]
	s_cbranch_vccz .LBB0_1430
	s_barrier

.LBB0_1772:
	s_add_u32 s43, s50, 0xfffc0080
	s_addc_u32 s52, s51, -1
	s_add_i32 s42, 0, 0x10000
	s_cmp_eq_u32 s68, 12
	s_cselect_b32 s55, s10, s52
	s_cselect_b32 s54, s11, s43
	s_cselect_b32 s53, s37, s67
	s_cselect_b32 s52, s39, s66
	s_add_i32 s43, 0, 0x14000
	ds_read_b128 v[20:23], v190
	ds_read_b128 v[28:31], v190 offset:2048
	ds_read_b128 v[24:27], v190 offset:1024
	ds_read_b128 v[32:35], v190 offset:3072
	ds_read_b128 v[4:7], v190 offset:16384
	ds_read_b128 v[12:15], v190 offset:18432
	ds_read_b128 v[8:11], v190 offset:17408
	ds_read_b128 v[16:19], v190 offset:19456
	v_lshl_add_u64 v[174:175], s[50:51], 0, v[170:171]
	s_add_i32 m0, s47, 0xc000
	ds_read_b128 v[178:181], v193
	ds_read_b128 v[196:199], v193 offset:2048
	ds_read_b128 v[182:185], v194
	ds_read_b128 v[200:203], v194 offset:2048
	ds_read_b128 v[204:207], v193 offset:4096
	ds_read_b128 v[226:229], v193 offset:6144
	ds_read_b128 v[208:211], v194 offset:4096
	ds_read_b128 v[230:233], v194 offset:6144
	global_load_lds_dwordx4 v[174:175], off
	v_lshl_add_u64 v[174:175], s[50:51], 0, v[172:173]
	s_add_i32 m0, s47, 0xe000
	s_nop 0
	global_load_lds_dwordx4 v[174:175], off
	s_waitcnt vmcnt(8)
	s_waitcnt lgkmcnt(0)
	s_setprio 1
	s_barrier
	v_mfma_scale_f32_16x16x128_f8f6f4 v[160:163], v[20:27], v[178:185], v[160:163], v219, v220 op_sel_hi:[0,0,0]
	v_mfma_scale_f32_16x16x128_f8f6f4 v[152:155], v[28:35], v[178:185], v[152:155], v219, v220 op_sel_hi:[0,0,0]
	v_mfma_scale_f32_16x16x128_f8f6f4 v[144:147], v[20:27], v[196:203], v[144:147], v219, v220 op_sel_hi:[0,0,0]
	v_mfma_scale_f32_16x16x128_f8f6f4 v[136:139], v[28:35], v[196:203], v[136:139], v219, v220 op_sel_hi:[0,0,0]
	v_mfma_scale_f32_16x16x128_f8f6f4 v[128:131], v[20:27], v[204:211], v[128:131], v219, v220 op_sel_hi:[0,0,0]
	v_mfma_scale_f32_16x16x128_f8f6f4 v[120:123], v[28:35], v[204:211], v[120:123], v219, v220 op_sel_hi:[0,0,0]
	v_mfma_scale_f32_16x16x128_f8f6f4 v[112:115], v[20:27], v[226:233], v[112:115], v219, v220 op_sel_hi:[0,0,0]
	v_mfma_scale_f32_16x16x128_f8f6f4 v[104:107], v[28:35], v[226:233], v[104:107], v219, v220 op_sel_hi:[0,0,0]
	s_setprio 0
	s_setprio 1
	v_mfma_scale_f32_16x16x128_f8f6f4 v[156:159], v[4:11], v[178:185], v[156:159], v219, v220 op_sel_hi:[0,0,0]
	v_mfma_scale_f32_16x16x128_f8f6f4 v[148:151], v[12:19], v[178:185], v[148:151], v219, v220 op_sel_hi:[0,0,0]
	v_mfma_scale_f32_16x16x128_f8f6f4 v[140:143], v[4:11], v[196:203], v[140:143], v219, v220 op_sel_hi:[0,0,0]
	v_mfma_scale_f32_16x16x128_f8f6f4 v[132:135], v[12:19], v[196:203], v[132:135], v219, v220 op_sel_hi:[0,0,0]
	v_mfma_scale_f32_16x16x128_f8f6f4 v[124:127], v[4:11], v[204:211], v[124:127], v219, v220 op_sel_hi:[0,0,0]
	v_mfma_scale_f32_16x16x128_f8f6f4 v[116:119], v[12:19], v[204:211], v[116:119], v219, v220 op_sel_hi:[0,0,0]
	v_mfma_scale_f32_16x16x128_f8f6f4 v[108:111], v[4:11], v[226:233], v[108:111], v219, v220 op_sel_hi:[0,0,0]
	v_mfma_scale_f32_16x16x128_f8f6f4 v[100:103], v[12:19], v[226:233], v[100:103], v219, v220 op_sel_hi:[0,0,0]
	s_setprio 0
	s_barrier
	s_add_i32 s42, s42, s57
	v_lshl_add_u64 v[182:183], s[52:53], 0, v[2:3]
	s_mov_b32 m0, s42
	ds_read_b128 v[196:199], v193 offset:16384
	ds_read_b128 v[204:207], v193 offset:18432
	ds_read_b128 v[200:203], v194 offset:16384
	ds_read_b128 v[208:211], v194 offset:18432
	ds_read_b128 v[226:229], v193 offset:20480
	ds_read_b128 v[234:237], v193 offset:22528
	ds_read_b128 v[230:233], v194 offset:20480
	ds_read_b128 v[238:241], v194 offset:22528
	global_load_lds_dwordx4 v[182:183], off
	s_add_i32 m0, s42, 0x2000
	s_add_u32 s70, s52, 0x40000
	v_lshl_add_u64 v[184:185], s[52:53], 0, v[164:165]
	s_addc_u32 s71, s53, 0
	s_add_i32 s42, s43, s57
	global_load_lds_dwordx4 v[184:185], off
	v_lshl_add_u64 v[174:175], s[70:71], 0, v[2:3]
	s_mov_b32 m0, s42
	v_lshl_add_u64 v[186:187], s[54:55], 0, v[168:169]
	global_load_lds_dwordx4 v[174:175], off
	v_lshl_add_u64 v[174:175], s[70:71], 0, v[164:165]
	s_add_i32 m0, s42, 0x2000
	v_lshl_add_u64 v[188:189], s[54:55], 0, v[166:167]
	global_load_lds_dwordx4 v[174:175], off
	s_mov_b32 m0, s47
	s_nop 0
	global_load_lds_dwordx4 v[186:187], off
	s_mov_b32 m0, s49
	s_nop 0
	global_load_lds_dwordx4 v[188:189], off
	s_waitcnt vmcnt(8)
	s_waitcnt lgkmcnt(0)
	s_setprio 1
	s_barrier
	v_mfma_scale_f32_16x16x128_f8f6f4 v[96:99], v[20:27], v[196:203], v[96:99], v219, v220 op_sel_hi:[0,0,0]
	v_mfma_scale_f32_16x16x128_f8f6f4 v[88:91], v[28:35], v[196:203], v[88:91], v219, v220 op_sel_hi:[0,0,0]
	v_mfma_scale_f32_16x16x128_f8f6f4 v[80:83], v[20:27], v[204:211], v[80:83], v219, v220 op_sel_hi:[0,0,0]
	v_mfma_scale_f32_16x16x128_f8f6f4 v[72:75], v[28:35], v[204:211], v[72:75], v219, v220 op_sel_hi:[0,0,0]
	v_mfma_scale_f32_16x16x128_f8f6f4 v[64:67], v[20:27], v[226:233], v[64:67], v219, v220 op_sel_hi:[0,0,0]
	v_mfma_scale_f32_16x16x128_f8f6f4 v[56:59], v[28:35], v[226:233], v[56:59], v219, v220 op_sel_hi:[0,0,0]
	v_mfma_scale_f32_16x16x128_f8f6f4 v[48:51], v[20:27], v[234:241], v[48:51], v219, v220 op_sel_hi:[0,0,0]
	v_mfma_scale_f32_16x16x128_f8f6f4 v[40:43], v[28:35], v[234:241], v[40:43], v219, v220 op_sel_hi:[0,0,0]
	s_setprio 0
	s_setprio 1
	v_mfma_scale_f32_16x16x128_f8f6f4 v[92:95], v[4:11], v[196:203], v[92:95], v219, v220 op_sel_hi:[0,0,0]
	v_mfma_scale_f32_16x16x128_f8f6f4 v[84:87], v[12:19], v[196:203], v[84:87], v219, v220 op_sel_hi:[0,0,0]
	v_mfma_scale_f32_16x16x128_f8f6f4 v[76:79], v[4:11], v[204:211], v[76:79], v219, v220 op_sel_hi:[0,0,0]
	v_mfma_scale_f32_16x16x128_f8f6f4 v[68:71], v[12:19], v[204:211], v[68:71], v219, v220 op_sel_hi:[0,0,0]
	v_mfma_scale_f32_16x16x128_f8f6f4 v[60:63], v[4:11], v[226:233], v[60:63], v219, v220 op_sel_hi:[0,0,0]
	v_mfma_scale_f32_16x16x128_f8f6f4 v[52:55], v[12:19], v[226:233], v[52:55], v219, v220 op_sel_hi:[0,0,0]
	v_mfma_scale_f32_16x16x128_f8f6f4 v[44:47], v[4:11], v[234:241], v[44:47], v219, v220 op_sel_hi:[0,0,0]
	v_mfma_scale_f32_16x16x128_f8f6f4 v[36:39], v[12:19], v[234:241], v[36:39], v219, v220 op_sel_hi:[0,0,0]
	s_setprio 0
	s_barrier
	s_add_i32 s69, 0, 0x18000
	s_add_i32 s70, 0, 0x1c000
	ds_read_b128 v[4:7], v190 offset:32768
	ds_read_b128 v[12:15], v190 offset:34816
	ds_read_b128 v[8:11], v190 offset:33792
	ds_read_b128 v[16:19], v190 offset:35840
	ds_read_b128 v[20:23], v190 offset:49152
	ds_read_b128 v[28:31], v190 offset:51200
	ds_read_b128 v[24:27], v190 offset:50176
	ds_read_b128 v[32:35], v190 offset:52224
	s_add_u32 s42, s54, 0x40000
	s_addc_u32 s43, s55, 0
	s_mov_b32 m0, s61
	v_lshl_add_u64 v[174:175], s[42:43], 0, v[168:169]
	ds_read_b128 v[196:199], v193 offset:32768
	ds_read_b128 v[204:207], v193 offset:34816
	ds_read_b128 v[200:203], v194 offset:32768
	ds_read_b128 v[208:211], v194 offset:34816
	ds_read_b128 v[226:229], v193 offset:36864
	ds_read_b128 v[234:237], v193 offset:38912
	ds_read_b128 v[230:233], v194 offset:36864
	ds_read_b128 v[238:241], v194 offset:38912
	global_load_lds_dwordx4 v[174:175], off
	v_lshl_add_u64 v[174:175], s[42:43], 0, v[166:167]
	s_mov_b32 m0, s62
	s_nop 0
	global_load_lds_dwordx4 v[174:175], off
	s_waitcnt vmcnt(8)
	s_waitcnt lgkmcnt(0)
	s_setprio 1
	s_barrier
	v_mfma_scale_f32_16x16x128_f8f6f4 v[160:163], v[4:11], v[196:203], v[160:163], v219, v220 op_sel_hi:[0,0,0]
	v_mfma_scale_f32_16x16x128_f8f6f4 v[152:155], v[12:19], v[196:203], v[152:155], v219, v220 op_sel_hi:[0,0,0]
	v_mfma_scale_f32_16x16x128_f8f6f4 v[144:147], v[4:11], v[204:211], v[144:147], v219, v220 op_sel_hi:[0,0,0]
	v_mfma_scale_f32_16x16x128_f8f6f4 v[136:139], v[12:19], v[204:211], v[136:139], v219, v220 op_sel_hi:[0,0,0]
	v_mfma_scale_f32_16x16x128_f8f6f4 v[128:131], v[4:11], v[226:233], v[128:131], v219, v220 op_sel_hi:[0,0,0]
	v_mfma_scale_f32_16x16x128_f8f6f4 v[120:123], v[12:19], v[226:233], v[120:123], v219, v220 op_sel_hi:[0,0,0]
	v_mfma_scale_f32_16x16x128_f8f6f4 v[112:115], v[4:11], v[234:241], v[112:115], v219, v220 op_sel_hi:[0,0,0]
	v_mfma_scale_f32_16x16x128_f8f6f4 v[104:107], v[12:19], v[234:241], v[104:107], v219, v220 op_sel_hi:[0,0,0]
	s_setprio 0
	s_setprio 1
	v_mfma_scale_f32_16x16x128_f8f6f4 v[156:159], v[20:27], v[196:203], v[156:159], v219, v220 op_sel_hi:[0,0,0]
	v_mfma_scale_f32_16x16x128_f8f6f4 v[148:151], v[28:35], v[196:203], v[148:151], v219, v220 op_sel_hi:[0,0,0]
	v_mfma_scale_f32_16x16x128_f8f6f4 v[140:143], v[20:27], v[204:211], v[140:143], v219, v220 op_sel_hi:[0,0,0]
	v_mfma_scale_f32_16x16x128_f8f6f4 v[132:135], v[28:35], v[204:211], v[132:135], v219, v220 op_sel_hi:[0,0,0]
	v_mfma_scale_f32_16x16x128_f8f6f4 v[124:127], v[20:27], v[226:233], v[124:127], v219, v220 op_sel_hi:[0,0,0]
	v_mfma_scale_f32_16x16x128_f8f6f4 v[116:119], v[28:35], v[226:233], v[116:119], v219, v220 op_sel_hi:[0,0,0]
	v_mfma_scale_f32_16x16x128_f8f6f4 v[108:111], v[20:27], v[234:241], v[108:111], v219, v220 op_sel_hi:[0,0,0]
	v_mfma_scale_f32_16x16x128_f8f6f4 v[100:103], v[28:35], v[234:241], v[100:103], v219, v220 op_sel_hi:[0,0,0]
	s_setprio 0
	s_barrier
	s_add_i32 s42, s69, s57
	v_lshl_add_u64 v[174:175], v[182:183], 0, s[6:7]
	s_mov_b32 m0, s42
	ds_read_b128 v[196:199], v193 offset:49152
	ds_read_b128 v[204:207], v193 offset:51200
	ds_read_b128 v[200:203], v194 offset:49152
	ds_read_b128 v[208:211], v194 offset:51200
	ds_read_b128 v[226:229], v193 offset:53248
	ds_read_b128 v[234:237], v193 offset:55296
	ds_read_b128 v[230:233], v194 offset:53248
	ds_read_b128 v[238:241], v194 offset:55296
	global_load_lds_dwordx4 v[174:175], off
	s_add_i32 m0, s42, 0x2000
	s_add_u32 s42, s52, 0x40080
	v_lshl_add_u64 v[174:175], v[184:185], 0, s[6:7]
	s_addc_u32 s43, s53, 0
	s_add_i32 s52, s70, s57
	global_load_lds_dwordx4 v[174:175], off
	v_lshl_add_u64 v[174:175], s[42:43], 0, v[2:3]
	s_mov_b32 m0, s52
	s_nop 0
	global_load_lds_dwordx4 v[174:175], off
	v_lshl_add_u64 v[174:175], s[42:43], 0, v[164:165]
	s_add_i32 m0, s52, 0x2000
	s_nop 0
	global_load_lds_dwordx4 v[174:175], off
	v_lshl_add_u64 v[174:175], v[186:187], 0, s[6:7]
	s_mov_b32 m0, s63
	s_nop 0
	global_load_lds_dwordx4 v[174:175], off
	v_lshl_add_u64 v[174:175], v[188:189], 0, s[6:7]
	s_mov_b32 m0, s64
	s_nop 0
	global_load_lds_dwordx4 v[174:175], off
	s_waitcnt vmcnt(8)
	s_waitcnt lgkmcnt(0)
	s_setprio 1
	s_barrier
	v_mfma_scale_f32_16x16x128_f8f6f4 v[96:99], v[4:11], v[196:203], v[96:99], v219, v220 op_sel_hi:[0,0,0]
	v_mfma_scale_f32_16x16x128_f8f6f4 v[88:91], v[12:19], v[196:203], v[88:91], v219, v220 op_sel_hi:[0,0,0]
	v_mfma_scale_f32_16x16x128_f8f6f4 v[80:83], v[4:11], v[204:211], v[80:83], v219, v220 op_sel_hi:[0,0,0]
	v_mfma_scale_f32_16x16x128_f8f6f4 v[72:75], v[12:19], v[204:211], v[72:75], v219, v220 op_sel_hi:[0,0,0]
	v_mfma_scale_f32_16x16x128_f8f6f4 v[64:67], v[4:11], v[226:233], v[64:67], v219, v220 op_sel_hi:[0,0,0]
	v_mfma_scale_f32_16x16x128_f8f6f4 v[56:59], v[12:19], v[226:233], v[56:59], v219, v220 op_sel_hi:[0,0,0]
	v_mfma_scale_f32_16x16x128_f8f6f4 v[48:51], v[4:11], v[234:241], v[48:51], v219, v220 op_sel_hi:[0,0,0]
	v_mfma_scale_f32_16x16x128_f8f6f4 v[40:43], v[12:19], v[234:241], v[40:43], v219, v220 op_sel_hi:[0,0,0]
	s_setprio 0
	s_setprio 1
	v_mfma_scale_f32_16x16x128_f8f6f4 v[92:95], v[20:27], v[196:203], v[92:95], v219, v220 op_sel_hi:[0,0,0]
	v_mfma_scale_f32_16x16x128_f8f6f4 v[84:87], v[28:35], v[196:203], v[84:87], v219, v220 op_sel_hi:[0,0,0]
	v_mfma_scale_f32_16x16x128_f8f6f4 v[76:79], v[20:27], v[204:211], v[76:79], v219, v220 op_sel_hi:[0,0,0]
	v_mfma_scale_f32_16x16x128_f8f6f4 v[68:71], v[28:35], v[204:211], v[68:71], v219, v220 op_sel_hi:[0,0,0]
	v_mfma_scale_f32_16x16x128_f8f6f4 v[60:63], v[20:27], v[226:233], v[60:63], v219, v220 op_sel_hi:[0,0,0]
	v_mfma_scale_f32_16x16x128_f8f6f4 v[52:55], v[28:35], v[226:233], v[52:55], v219, v220 op_sel_hi:[0,0,0]
	v_mfma_scale_f32_16x16x128_f8f6f4 v[44:47], v[20:27], v[234:241], v[44:47], v219, v220 op_sel_hi:[0,0,0]
	v_mfma_scale_f32_16x16x128_f8f6f4 v[36:39], v[28:35], v[234:241], v[36:39], v219, v220 op_sel_hi:[0,0,0]
	s_setprio 0
	s_barrier
	s_add_i32 s68, s68, 2
	s_add_u32 s50, s50, 0x100
	s_addc_u32 s51, s51, 0
	s_add_u32 s66, s66, 0x100
	s_addc_u32 s67, s67, 0
	s_cmp_gt_u32 s68, 13
	s_cbranch_scc0 .LBB0_1772
	s_nop 15
	s_nop 15
	s_and_b64 vcc, exec, s[14:15]
	s_cbranch_vccz .LBB0_1775
	s_barrier

.LBB0_1812:
	s_add_u32 s43, s52, 0xfffc0080
	s_addc_u32 s54, s53, -1
	s_add_i32 s42, 0, 0x10000
	s_cmp_eq_u32 s79, 12
	s_cselect_b32 s57, s10, s54
	s_cselect_b32 s56, s11, s43
	s_cselect_b32 s55, s39, s78
	s_cselect_b32 s54, s41, s77
	s_add_i32 s43, 0, 0x14000
	ds_read_b128 v[20:23], v190
	ds_read_b128 v[28:31], v190 offset:2048
	ds_read_b128 v[24:27], v190 offset:1024
	ds_read_b128 v[32:35], v190 offset:3072
	ds_read_b128 v[4:7], v190 offset:16384
	ds_read_b128 v[12:15], v190 offset:18432
	ds_read_b128 v[8:11], v190 offset:17408
	ds_read_b128 v[16:19], v190 offset:19456
	v_lshl_add_u64 v[174:175], s[52:53], 0, v[170:171]
	s_add_i32 m0, s49, 0xc000
	ds_read_b128 v[178:181], v193
	ds_read_b128 v[196:199], v193 offset:2048
	ds_read_b128 v[182:185], v194
	ds_read_b128 v[200:203], v194 offset:2048
	ds_read_b128 v[204:207], v193 offset:4096
	ds_read_b128 v[226:229], v193 offset:6144
	ds_read_b128 v[208:211], v194 offset:4096
	ds_read_b128 v[230:233], v194 offset:6144
	global_load_lds_dwordx4 v[174:175], off
	v_lshl_add_u64 v[174:175], s[52:53], 0, v[172:173]
	s_add_i32 m0, s49, 0xe000
	s_nop 0
	global_load_lds_dwordx4 v[174:175], off
	s_waitcnt vmcnt(8)
	s_waitcnt lgkmcnt(0)
	s_setprio 1
	s_barrier
	v_mfma_scale_f32_16x16x128_f8f6f4 v[160:163], v[20:27], v[178:185], v[160:163], v219, v220 op_sel_hi:[0,0,0]
	v_mfma_scale_f32_16x16x128_f8f6f4 v[152:155], v[28:35], v[178:185], v[152:155], v219, v220 op_sel_hi:[0,0,0]
	v_mfma_scale_f32_16x16x128_f8f6f4 v[144:147], v[20:27], v[196:203], v[144:147], v219, v220 op_sel_hi:[0,0,0]
	v_mfma_scale_f32_16x16x128_f8f6f4 v[136:139], v[28:35], v[196:203], v[136:139], v219, v220 op_sel_hi:[0,0,0]
	v_mfma_scale_f32_16x16x128_f8f6f4 v[128:131], v[20:27], v[204:211], v[128:131], v219, v220 op_sel_hi:[0,0,0]
	v_mfma_scale_f32_16x16x128_f8f6f4 v[120:123], v[28:35], v[204:211], v[120:123], v219, v220 op_sel_hi:[0,0,0]
	v_mfma_scale_f32_16x16x128_f8f6f4 v[112:115], v[20:27], v[226:233], v[112:115], v219, v220 op_sel_hi:[0,0,0]
	v_mfma_scale_f32_16x16x128_f8f6f4 v[104:107], v[28:35], v[226:233], v[104:107], v219, v220 op_sel_hi:[0,0,0]
	s_setprio 0
	s_setprio 1
	v_mfma_scale_f32_16x16x128_f8f6f4 v[156:159], v[4:11], v[178:185], v[156:159], v219, v220 op_sel_hi:[0,0,0]
	v_mfma_scale_f32_16x16x128_f8f6f4 v[148:151], v[12:19], v[178:185], v[148:151], v219, v220 op_sel_hi:[0,0,0]
	v_mfma_scale_f32_16x16x128_f8f6f4 v[140:143], v[4:11], v[196:203], v[140:143], v219, v220 op_sel_hi:[0,0,0]
	v_mfma_scale_f32_16x16x128_f8f6f4 v[132:135], v[12:19], v[196:203], v[132:135], v219, v220 op_sel_hi:[0,0,0]
	v_mfma_scale_f32_16x16x128_f8f6f4 v[124:127], v[4:11], v[204:211], v[124:127], v219, v220 op_sel_hi:[0,0,0]
	v_mfma_scale_f32_16x16x128_f8f6f4 v[116:119], v[12:19], v[204:211], v[116:119], v219, v220 op_sel_hi:[0,0,0]
	v_mfma_scale_f32_16x16x128_f8f6f4 v[108:111], v[4:11], v[226:233], v[108:111], v219, v220 op_sel_hi:[0,0,0]
	v_mfma_scale_f32_16x16x128_f8f6f4 v[100:103], v[12:19], v[226:233], v[100:103], v219, v220 op_sel_hi:[0,0,0]
	s_setprio 0
	s_barrier
	s_add_i32 s42, s42, s69
	v_lshl_add_u64 v[182:183], s[54:55], 0, v[2:3]
	s_mov_b32 m0, s42
	ds_read_b128 v[196:199], v193 offset:16384
	ds_read_b128 v[204:207], v193 offset:18432
	ds_read_b128 v[200:203], v194 offset:16384
	ds_read_b128 v[208:211], v194 offset:18432
	ds_read_b128 v[226:229], v193 offset:20480
	ds_read_b128 v[234:237], v193 offset:22528
	ds_read_b128 v[230:233], v194 offset:20480
	ds_read_b128 v[238:241], v194 offset:22528
	global_load_lds_dwordx4 v[182:183], off
	s_add_i32 m0, s42, 0x2000
	s_add_u32 s80, s54, 0x40000
	v_lshl_add_u64 v[184:185], s[54:55], 0, v[168:169]
	s_addc_u32 s81, s55, 0
	s_add_i32 s42, s43, s69
	global_load_lds_dwordx4 v[184:185], off
	v_lshl_add_u64 v[174:175], s[80:81], 0, v[2:3]
	s_mov_b32 m0, s42
	v_lshl_add_u64 v[186:187], s[56:57], 0, v[164:165]
	global_load_lds_dwordx4 v[174:175], off
	v_lshl_add_u64 v[174:175], s[80:81], 0, v[168:169]
	s_add_i32 m0, s42, 0x2000
	v_lshl_add_u64 v[188:189], s[56:57], 0, v[166:167]
	global_load_lds_dwordx4 v[174:175], off
	s_mov_b32 m0, s49
	s_nop 0
	global_load_lds_dwordx4 v[186:187], off
	s_mov_b32 m0, s51
	s_nop 0
	global_load_lds_dwordx4 v[188:189], off
	s_waitcnt vmcnt(8)
	s_waitcnt lgkmcnt(0)
	s_setprio 1
	s_barrier
	v_mfma_scale_f32_16x16x128_f8f6f4 v[96:99], v[20:27], v[196:203], v[96:99], v219, v220 op_sel_hi:[0,0,0]
	v_mfma_scale_f32_16x16x128_f8f6f4 v[88:91], v[28:35], v[196:203], v[88:91], v219, v220 op_sel_hi:[0,0,0]
	v_mfma_scale_f32_16x16x128_f8f6f4 v[80:83], v[20:27], v[204:211], v[80:83], v219, v220 op_sel_hi:[0,0,0]
	v_mfma_scale_f32_16x16x128_f8f6f4 v[72:75], v[28:35], v[204:211], v[72:75], v219, v220 op_sel_hi:[0,0,0]
	v_mfma_scale_f32_16x16x128_f8f6f4 v[64:67], v[20:27], v[226:233], v[64:67], v219, v220 op_sel_hi:[0,0,0]
	v_mfma_scale_f32_16x16x128_f8f6f4 v[56:59], v[28:35], v[226:233], v[56:59], v219, v220 op_sel_hi:[0,0,0]
	v_mfma_scale_f32_16x16x128_f8f6f4 v[48:51], v[20:27], v[234:241], v[48:51], v219, v220 op_sel_hi:[0,0,0]
	v_mfma_scale_f32_16x16x128_f8f6f4 v[40:43], v[28:35], v[234:241], v[40:43], v219, v220 op_sel_hi:[0,0,0]
	s_setprio 0
	s_setprio 1
	v_mfma_scale_f32_16x16x128_f8f6f4 v[92:95], v[4:11], v[196:203], v[92:95], v219, v220 op_sel_hi:[0,0,0]
	v_mfma_scale_f32_16x16x128_f8f6f4 v[84:87], v[12:19], v[196:203], v[84:87], v219, v220 op_sel_hi:[0,0,0]
	v_mfma_scale_f32_16x16x128_f8f6f4 v[76:79], v[4:11], v[204:211], v[76:79], v219, v220 op_sel_hi:[0,0,0]
	v_mfma_scale_f32_16x16x128_f8f6f4 v[68:71], v[12:19], v[204:211], v[68:71], v219, v220 op_sel_hi:[0,0,0]
	v_mfma_scale_f32_16x16x128_f8f6f4 v[60:63], v[4:11], v[226:233], v[60:63], v219, v220 op_sel_hi:[0,0,0]
	v_mfma_scale_f32_16x16x128_f8f6f4 v[52:55], v[12:19], v[226:233], v[52:55], v219, v220 op_sel_hi:[0,0,0]
	v_mfma_scale_f32_16x16x128_f8f6f4 v[44:47], v[4:11], v[234:241], v[44:47], v219, v220 op_sel_hi:[0,0,0]
	v_mfma_scale_f32_16x16x128_f8f6f4 v[36:39], v[12:19], v[234:241], v[36:39], v219, v220 op_sel_hi:[0,0,0]
	s_setprio 0
	s_barrier
	s_add_i32 s80, 0, 0x18000
	s_add_i32 s81, 0, 0x1c000
	ds_read_b128 v[4:7], v190 offset:32768
	ds_read_b128 v[12:15], v190 offset:34816
	ds_read_b128 v[8:11], v190 offset:33792
	ds_read_b128 v[16:19], v190 offset:35840
	ds_read_b128 v[20:23], v190 offset:49152
	ds_read_b128 v[28:31], v190 offset:51200
	ds_read_b128 v[24:27], v190 offset:50176
	ds_read_b128 v[32:35], v190 offset:52224
	s_add_u32 s42, s56, 0x40000
	s_addc_u32 s43, s57, 0
	s_mov_b32 m0, s72
	v_lshl_add_u64 v[174:175], s[42:43], 0, v[164:165]
	ds_read_b128 v[196:199], v193 offset:32768
	ds_read_b128 v[204:207], v193 offset:34816
	ds_read_b128 v[200:203], v194 offset:32768
	ds_read_b128 v[208:211], v194 offset:34816
	ds_read_b128 v[226:229], v193 offset:36864
	ds_read_b128 v[234:237], v193 offset:38912
	ds_read_b128 v[230:233], v194 offset:36864
	ds_read_b128 v[238:241], v194 offset:38912
	global_load_lds_dwordx4 v[174:175], off
	v_lshl_add_u64 v[174:175], s[42:43], 0, v[166:167]
	s_mov_b32 m0, s73
	s_nop 0
	global_load_lds_dwordx4 v[174:175], off
	s_waitcnt vmcnt(8)
	s_waitcnt lgkmcnt(0)
	s_setprio 1
	s_barrier
	v_mfma_scale_f32_16x16x128_f8f6f4 v[160:163], v[4:11], v[196:203], v[160:163], v219, v220 op_sel_hi:[0,0,0]
	v_mfma_scale_f32_16x16x128_f8f6f4 v[152:155], v[12:19], v[196:203], v[152:155], v219, v220 op_sel_hi:[0,0,0]
	v_mfma_scale_f32_16x16x128_f8f6f4 v[144:147], v[4:11], v[204:211], v[144:147], v219, v220 op_sel_hi:[0,0,0]
	v_mfma_scale_f32_16x16x128_f8f6f4 v[136:139], v[12:19], v[204:211], v[136:139], v219, v220 op_sel_hi:[0,0,0]
	v_mfma_scale_f32_16x16x128_f8f6f4 v[128:131], v[4:11], v[226:233], v[128:131], v219, v220 op_sel_hi:[0,0,0]
	v_mfma_scale_f32_16x16x128_f8f6f4 v[120:123], v[12:19], v[226:233], v[120:123], v219, v220 op_sel_hi:[0,0,0]
	v_mfma_scale_f32_16x16x128_f8f6f4 v[112:115], v[4:11], v[234:241], v[112:115], v219, v220 op_sel_hi:[0,0,0]
	v_mfma_scale_f32_16x16x128_f8f6f4 v[104:107], v[12:19], v[234:241], v[104:107], v219, v220 op_sel_hi:[0,0,0]
	s_setprio 0
	s_setprio 1
	v_mfma_scale_f32_16x16x128_f8f6f4 v[156:159], v[20:27], v[196:203], v[156:159], v219, v220 op_sel_hi:[0,0,0]
	v_mfma_scale_f32_16x16x128_f8f6f4 v[148:151], v[28:35], v[196:203], v[148:151], v219, v220 op_sel_hi:[0,0,0]
	v_mfma_scale_f32_16x16x128_f8f6f4 v[140:143], v[20:27], v[204:211], v[140:143], v219, v220 op_sel_hi:[0,0,0]
	v_mfma_scale_f32_16x16x128_f8f6f4 v[132:135], v[28:35], v[204:211], v[132:135], v219, v220 op_sel_hi:[0,0,0]
	v_mfma_scale_f32_16x16x128_f8f6f4 v[124:127], v[20:27], v[226:233], v[124:127], v219, v220 op_sel_hi:[0,0,0]
	v_mfma_scale_f32_16x16x128_f8f6f4 v[116:119], v[28:35], v[226:233], v[116:119], v219, v220 op_sel_hi:[0,0,0]
	v_mfma_scale_f32_16x16x128_f8f6f4 v[108:111], v[20:27], v[234:241], v[108:111], v219, v220 op_sel_hi:[0,0,0]
	v_mfma_scale_f32_16x16x128_f8f6f4 v[100:103], v[28:35], v[234:241], v[100:103], v219, v220 op_sel_hi:[0,0,0]
	s_setprio 0
	s_barrier
	s_add_i32 s42, s80, s69
	v_lshl_add_u64 v[174:175], v[182:183], 0, s[6:7]
	s_mov_b32 m0, s42
	ds_read_b128 v[196:199], v193 offset:49152
	ds_read_b128 v[204:207], v193 offset:51200
	ds_read_b128 v[200:203], v194 offset:49152
	ds_read_b128 v[208:211], v194 offset:51200
	ds_read_b128 v[226:229], v193 offset:53248
	ds_read_b128 v[234:237], v193 offset:55296
	ds_read_b128 v[230:233], v194 offset:53248
	ds_read_b128 v[238:241], v194 offset:55296
	global_load_lds_dwordx4 v[174:175], off
	s_add_i32 m0, s42, 0x2000
	s_add_u32 s42, s54, 0x40080
	v_lshl_add_u64 v[174:175], v[184:185], 0, s[6:7]
	s_addc_u32 s43, s55, 0
	s_add_i32 s54, s81, s69
	global_load_lds_dwordx4 v[174:175], off
	v_lshl_add_u64 v[174:175], s[42:43], 0, v[2:3]
	s_mov_b32 m0, s54
	s_nop 0
	global_load_lds_dwordx4 v[174:175], off
	v_lshl_add_u64 v[174:175], s[42:43], 0, v[168:169]
	s_add_i32 m0, s54, 0x2000
	s_nop 0
	global_load_lds_dwordx4 v[174:175], off
	v_lshl_add_u64 v[174:175], v[186:187], 0, s[6:7]
	s_mov_b32 m0, s74
	s_nop 0
	global_load_lds_dwordx4 v[174:175], off
	v_lshl_add_u64 v[174:175], v[188:189], 0, s[6:7]
	s_mov_b32 m0, s75
	s_nop 0
	global_load_lds_dwordx4 v[174:175], off
	s_waitcnt vmcnt(8)
	s_waitcnt lgkmcnt(0)
	s_setprio 1
	s_barrier
	v_mfma_scale_f32_16x16x128_f8f6f4 v[96:99], v[4:11], v[196:203], v[96:99], v219, v220 op_sel_hi:[0,0,0]
	v_mfma_scale_f32_16x16x128_f8f6f4 v[88:91], v[12:19], v[196:203], v[88:91], v219, v220 op_sel_hi:[0,0,0]
	v_mfma_scale_f32_16x16x128_f8f6f4 v[80:83], v[4:11], v[204:211], v[80:83], v219, v220 op_sel_hi:[0,0,0]
	v_mfma_scale_f32_16x16x128_f8f6f4 v[72:75], v[12:19], v[204:211], v[72:75], v219, v220 op_sel_hi:[0,0,0]
	v_mfma_scale_f32_16x16x128_f8f6f4 v[64:67], v[4:11], v[226:233], v[64:67], v219, v220 op_sel_hi:[0,0,0]
	v_mfma_scale_f32_16x16x128_f8f6f4 v[56:59], v[12:19], v[226:233], v[56:59], v219, v220 op_sel_hi:[0,0,0]
	v_mfma_scale_f32_16x16x128_f8f6f4 v[48:51], v[4:11], v[234:241], v[48:51], v219, v220 op_sel_hi:[0,0,0]
	v_mfma_scale_f32_16x16x128_f8f6f4 v[40:43], v[12:19], v[234:241], v[40:43], v219, v220 op_sel_hi:[0,0,0]
	s_setprio 0
	s_setprio 1
	v_mfma_scale_f32_16x16x128_f8f6f4 v[92:95], v[20:27], v[196:203], v[92:95], v219, v220 op_sel_hi:[0,0,0]
	v_mfma_scale_f32_16x16x128_f8f6f4 v[84:87], v[28:35], v[196:203], v[84:87], v219, v220 op_sel_hi:[0,0,0]
	v_mfma_scale_f32_16x16x128_f8f6f4 v[76:79], v[20:27], v[204:211], v[76:79], v219, v220 op_sel_hi:[0,0,0]
	v_mfma_scale_f32_16x16x128_f8f6f4 v[68:71], v[28:35], v[204:211], v[68:71], v219, v220 op_sel_hi:[0,0,0]
	v_mfma_scale_f32_16x16x128_f8f6f4 v[60:63], v[20:27], v[226:233], v[60:63], v219, v220 op_sel_hi:[0,0,0]
	v_mfma_scale_f32_16x16x128_f8f6f4 v[52:55], v[28:35], v[226:233], v[52:55], v219, v220 op_sel_hi:[0,0,0]
	v_mfma_scale_f32_16x16x128_f8f6f4 v[44:47], v[20:27], v[234:241], v[44:47], v219, v220 op_sel_hi:[0,0,0]
	v_mfma_scale_f32_16x16x128_f8f6f4 v[36:39], v[28:35], v[234:241], v[36:39], v219, v220 op_sel_hi:[0,0,0]
	s_setprio 0
	s_barrier
	s_add_i32 s79, s79, 2
	s_add_u32 s52, s52, 0x100
	s_addc_u32 s53, s53, 0
	s_add_u32 s77, s77, 0x100
	s_addc_u32 s78, s78, 0
	s_cmp_gt_u32 s79, 13
	s_cbranch_scc0 .LBB0_1812
	s_nop 15
	s_nop 15
	s_and_b64 vcc, exec, s[36:37]
	v_readlane_b32 s78, v249, 36
	s_mov_b32 s79, s28
	s_cbranch_vccz .LBB0_1815
	s_barrier

.LBB0_1894:
	s_add_u32 s43, s40, 0xfff50080
	s_addc_u32 s44, s41, -1
	s_add_i32 s42, 0, 0x10000
	s_cmp_eq_u32 s61, 40
	s_cselect_b32 s47, s5, s44
	s_cselect_b32 s46, s4, s43
	s_cselect_b32 s45, s39, s60
	s_cselect_b32 s44, s38, s59
	s_add_i32 s43, 0, 0x14000
	ds_read_b128 v[20:23], v190
	ds_read_b128 v[28:31], v190 offset:2048
	ds_read_b128 v[24:27], v190 offset:1024
	ds_read_b128 v[32:35], v190 offset:3072
	ds_read_b128 v[4:7], v190 offset:16384
	ds_read_b128 v[12:15], v190 offset:18432
	ds_read_b128 v[8:11], v190 offset:17408
	ds_read_b128 v[16:19], v190 offset:19456
	v_lshl_add_u64 v[174:175], s[40:41], 0, v[170:171]
	s_add_i32 m0, s11, 0xc000
	ds_read_b128 v[178:181], v193
	ds_read_b128 v[196:199], v193 offset:2048
	ds_read_b128 v[182:185], v194
	ds_read_b128 v[200:203], v194 offset:2048
	ds_read_b128 v[204:207], v193 offset:4096
	ds_read_b128 v[226:229], v193 offset:6144
	ds_read_b128 v[208:211], v194 offset:4096
	ds_read_b128 v[230:233], v194 offset:6144
	global_load_lds_dwordx4 v[174:175], off
	v_lshl_add_u64 v[174:175], s[40:41], 0, v[172:173]
	s_add_i32 m0, s11, 0xe000
	s_nop 0
	global_load_lds_dwordx4 v[174:175], off
	s_waitcnt vmcnt(8)
	s_waitcnt lgkmcnt(0)
	s_setprio 1
	s_barrier
	v_mfma_scale_f32_16x16x128_f8f6f4 v[160:163], v[20:27], v[178:185], v[160:163], v219, v220 op_sel_hi:[0,0,0]
	v_mfma_scale_f32_16x16x128_f8f6f4 v[156:159], v[28:35], v[178:185], v[156:159], v219, v220 op_sel_hi:[0,0,0]
	v_mfma_scale_f32_16x16x128_f8f6f4 v[152:155], v[20:27], v[196:203], v[152:155], v219, v220 op_sel_hi:[0,0,0]
	v_mfma_scale_f32_16x16x128_f8f6f4 v[148:151], v[28:35], v[196:203], v[148:151], v219, v220 op_sel_hi:[0,0,0]
	v_mfma_scale_f32_16x16x128_f8f6f4 v[136:139], v[20:27], v[204:211], v[136:139], v219, v220 op_sel_hi:[0,0,0]
	v_mfma_scale_f32_16x16x128_f8f6f4 v[132:135], v[28:35], v[204:211], v[132:135], v219, v220 op_sel_hi:[0,0,0]
	v_mfma_scale_f32_16x16x128_f8f6f4 v[120:123], v[20:27], v[226:233], v[120:123], v219, v220 op_sel_hi:[0,0,0]
	v_mfma_scale_f32_16x16x128_f8f6f4 v[116:119], v[28:35], v[226:233], v[116:119], v219, v220 op_sel_hi:[0,0,0]
	s_setprio 0
	s_setprio 1
	v_mfma_scale_f32_16x16x128_f8f6f4 v[144:147], v[4:11], v[178:185], v[144:147], v219, v220 op_sel_hi:[0,0,0]
	v_mfma_scale_f32_16x16x128_f8f6f4 v[140:143], v[12:19], v[178:185], v[140:143], v219, v220 op_sel_hi:[0,0,0]
	v_mfma_scale_f32_16x16x128_f8f6f4 v[128:131], v[4:11], v[196:203], v[128:131], v219, v220 op_sel_hi:[0,0,0]
	v_mfma_scale_f32_16x16x128_f8f6f4 v[124:127], v[12:19], v[196:203], v[124:127], v219, v220 op_sel_hi:[0,0,0]
	v_mfma_scale_f32_16x16x128_f8f6f4 v[112:115], v[4:11], v[204:211], v[112:115], v219, v220 op_sel_hi:[0,0,0]
	v_mfma_scale_f32_16x16x128_f8f6f4 v[108:111], v[12:19], v[204:211], v[108:111], v219, v220 op_sel_hi:[0,0,0]
	v_mfma_scale_f32_16x16x128_f8f6f4 v[104:107], v[4:11], v[226:233], v[104:107], v219, v220 op_sel_hi:[0,0,0]
	v_mfma_scale_f32_16x16x128_f8f6f4 v[100:103], v[12:19], v[226:233], v[100:103], v219, v220 op_sel_hi:[0,0,0]
	s_setprio 0
	s_barrier
	s_add_i32 s42, s42, s10
	v_lshl_add_u64 v[182:183], s[44:45], 0, v[2:3]
	s_mov_b32 m0, s42
	ds_read_b128 v[196:199], v193 offset:16384
	ds_read_b128 v[204:207], v193 offset:18432
	ds_read_b128 v[200:203], v194 offset:16384
	ds_read_b128 v[208:211], v194 offset:18432
	ds_read_b128 v[226:229], v193 offset:20480
	ds_read_b128 v[234:237], v193 offset:22528
	ds_read_b128 v[230:233], v194 offset:20480
	ds_read_b128 v[238:241], v194 offset:22528
	global_load_lds_dwordx4 v[182:183], off
	s_add_i32 m0, s42, 0x2000
	s_add_u32 s62, s44, 0xb0000
	v_lshl_add_u64 v[184:185], s[44:45], 0, v[164:165]
	s_addc_u32 s63, s45, 0
	s_add_i32 s42, s43, s10
	global_load_lds_dwordx4 v[184:185], off
	v_lshl_add_u64 v[174:175], s[62:63], 0, v[2:3]
	s_mov_b32 m0, s42
	v_lshl_add_u64 v[186:187], s[46:47], 0, v[168:169]
	global_load_lds_dwordx4 v[174:175], off
	v_lshl_add_u64 v[174:175], s[62:63], 0, v[164:165]
	s_add_i32 m0, s42, 0x2000
	v_lshl_add_u64 v[188:189], s[46:47], 0, v[166:167]
	global_load_lds_dwordx4 v[174:175], off
	s_mov_b32 m0, s11
	s_nop 0
	global_load_lds_dwordx4 v[186:187], off
	s_mov_b32 m0, s12
	s_nop 0
	global_load_lds_dwordx4 v[188:189], off
	s_waitcnt vmcnt(8)
	s_waitcnt lgkmcnt(0)
	s_setprio 1
	s_barrier
	v_mfma_scale_f32_16x16x128_f8f6f4 v[96:99], v[20:27], v[196:203], v[96:99], v219, v220 op_sel_hi:[0,0,0]
	v_mfma_scale_f32_16x16x128_f8f6f4 v[92:95], v[28:35], v[196:203], v[92:95], v219, v220 op_sel_hi:[0,0,0]
	v_mfma_scale_f32_16x16x128_f8f6f4 v[88:91], v[20:27], v[204:211], v[88:91], v219, v220 op_sel_hi:[0,0,0]
	v_mfma_scale_f32_16x16x128_f8f6f4 v[84:87], v[28:35], v[204:211], v[84:87], v219, v220 op_sel_hi:[0,0,0]
	v_mfma_scale_f32_16x16x128_f8f6f4 v[72:75], v[20:27], v[226:233], v[72:75], v219, v220 op_sel_hi:[0,0,0]
	v_mfma_scale_f32_16x16x128_f8f6f4 v[68:71], v[28:35], v[226:233], v[68:71], v219, v220 op_sel_hi:[0,0,0]
	v_mfma_scale_f32_16x16x128_f8f6f4 v[56:59], v[20:27], v[234:241], v[56:59], v219, v220 op_sel_hi:[0,0,0]
	v_mfma_scale_f32_16x16x128_f8f6f4 v[52:55], v[28:35], v[234:241], v[52:55], v219, v220 op_sel_hi:[0,0,0]
	s_setprio 0
	s_setprio 1
	v_mfma_scale_f32_16x16x128_f8f6f4 v[80:83], v[4:11], v[196:203], v[80:83], v219, v220 op_sel_hi:[0,0,0]
	v_mfma_scale_f32_16x16x128_f8f6f4 v[76:79], v[12:19], v[196:203], v[76:79], v219, v220 op_sel_hi:[0,0,0]
	v_mfma_scale_f32_16x16x128_f8f6f4 v[64:67], v[4:11], v[204:211], v[64:67], v219, v220 op_sel_hi:[0,0,0]
	v_mfma_scale_f32_16x16x128_f8f6f4 v[60:63], v[12:19], v[204:211], v[60:63], v219, v220 op_sel_hi:[0,0,0]
	v_mfma_scale_f32_16x16x128_f8f6f4 v[48:51], v[4:11], v[226:233], v[48:51], v219, v220 op_sel_hi:[0,0,0]
	v_mfma_scale_f32_16x16x128_f8f6f4 v[44:47], v[12:19], v[226:233], v[44:47], v219, v220 op_sel_hi:[0,0,0]
	v_mfma_scale_f32_16x16x128_f8f6f4 v[40:43], v[4:11], v[234:241], v[40:43], v219, v220 op_sel_hi:[0,0,0]
	v_mfma_scale_f32_16x16x128_f8f6f4 v[36:39], v[12:19], v[234:241], v[36:39], v219, v220 op_sel_hi:[0,0,0]
	s_setprio 0
	s_barrier
	s_add_i32 s62, 0, 0x18000
	s_add_i32 s63, 0, 0x1c000
	ds_read_b128 v[4:7], v190 offset:32768
	ds_read_b128 v[12:15], v190 offset:34816
	ds_read_b128 v[8:11], v190 offset:33792
	ds_read_b128 v[16:19], v190 offset:35840
	ds_read_b128 v[20:23], v190 offset:49152
	ds_read_b128 v[28:31], v190 offset:51200
	ds_read_b128 v[24:27], v190 offset:50176
	ds_read_b128 v[32:35], v190 offset:52224
	s_add_u32 s42, s46, 0xb0000
	s_addc_u32 s43, s47, 0
	s_mov_b32 m0, s48
	v_lshl_add_u64 v[174:175], s[42:43], 0, v[168:169]
	ds_read_b128 v[196:199], v193 offset:32768
	ds_read_b128 v[204:207], v193 offset:34816
	ds_read_b128 v[200:203], v194 offset:32768
	ds_read_b128 v[208:211], v194 offset:34816
	ds_read_b128 v[226:229], v193 offset:36864
	ds_read_b128 v[234:237], v193 offset:38912
	ds_read_b128 v[230:233], v194 offset:36864
	ds_read_b128 v[238:241], v194 offset:38912
	global_load_lds_dwordx4 v[174:175], off
	v_lshl_add_u64 v[174:175], s[42:43], 0, v[166:167]
	s_mov_b32 m0, s49
	s_nop 0
	global_load_lds_dwordx4 v[174:175], off
	s_waitcnt vmcnt(8)
	s_waitcnt lgkmcnt(0)
	s_setprio 1
	s_barrier
	v_mfma_scale_f32_16x16x128_f8f6f4 v[160:163], v[4:11], v[196:203], v[160:163], v219, v220 op_sel_hi:[0,0,0]
	v_mfma_scale_f32_16x16x128_f8f6f4 v[156:159], v[12:19], v[196:203], v[156:159], v219, v220 op_sel_hi:[0,0,0]
	v_mfma_scale_f32_16x16x128_f8f6f4 v[152:155], v[4:11], v[204:211], v[152:155], v219, v220 op_sel_hi:[0,0,0]
	v_mfma_scale_f32_16x16x128_f8f6f4 v[148:151], v[12:19], v[204:211], v[148:151], v219, v220 op_sel_hi:[0,0,0]
	v_mfma_scale_f32_16x16x128_f8f6f4 v[136:139], v[4:11], v[226:233], v[136:139], v219, v220 op_sel_hi:[0,0,0]
	v_mfma_scale_f32_16x16x128_f8f6f4 v[132:135], v[12:19], v[226:233], v[132:135], v219, v220 op_sel_hi:[0,0,0]
	v_mfma_scale_f32_16x16x128_f8f6f4 v[120:123], v[4:11], v[234:241], v[120:123], v219, v220 op_sel_hi:[0,0,0]
	v_mfma_scale_f32_16x16x128_f8f6f4 v[116:119], v[12:19], v[234:241], v[116:119], v219, v220 op_sel_hi:[0,0,0]
	s_setprio 0
	s_setprio 1
	v_mfma_scale_f32_16x16x128_f8f6f4 v[144:147], v[20:27], v[196:203], v[144:147], v219, v220 op_sel_hi:[0,0,0]
	v_mfma_scale_f32_16x16x128_f8f6f4 v[140:143], v[28:35], v[196:203], v[140:143], v219, v220 op_sel_hi:[0,0,0]
	v_mfma_scale_f32_16x16x128_f8f6f4 v[128:131], v[20:27], v[204:211], v[128:131], v219, v220 op_sel_hi:[0,0,0]
	v_mfma_scale_f32_16x16x128_f8f6f4 v[124:127], v[28:35], v[204:211], v[124:127], v219, v220 op_sel_hi:[0,0,0]
	v_mfma_scale_f32_16x16x128_f8f6f4 v[112:115], v[20:27], v[226:233], v[112:115], v219, v220 op_sel_hi:[0,0,0]
	v_mfma_scale_f32_16x16x128_f8f6f4 v[108:111], v[28:35], v[226:233], v[108:111], v219, v220 op_sel_hi:[0,0,0]
	v_mfma_scale_f32_16x16x128_f8f6f4 v[104:107], v[20:27], v[234:241], v[104:107], v219, v220 op_sel_hi:[0,0,0]
	v_mfma_scale_f32_16x16x128_f8f6f4 v[100:103], v[28:35], v[234:241], v[100:103], v219, v220 op_sel_hi:[0,0,0]
	s_setprio 0
	s_barrier
	s_add_i32 s42, s62, s10
	v_lshl_add_u64 v[174:175], v[182:183], 0, s[6:7]
	s_mov_b32 m0, s42
	ds_read_b128 v[196:199], v193 offset:49152
	ds_read_b128 v[204:207], v193 offset:51200
	ds_read_b128 v[200:203], v194 offset:49152
	ds_read_b128 v[208:211], v194 offset:51200
	ds_read_b128 v[226:229], v193 offset:53248
	ds_read_b128 v[234:237], v193 offset:55296
	ds_read_b128 v[230:233], v194 offset:53248
	ds_read_b128 v[238:241], v194 offset:55296
	global_load_lds_dwordx4 v[174:175], off
	s_add_i32 m0, s42, 0x2000
	s_add_u32 s42, s44, 0xb0080
	v_lshl_add_u64 v[174:175], v[184:185], 0, s[6:7]
	s_addc_u32 s43, s45, 0
	s_add_i32 s44, s63, s10
	global_load_lds_dwordx4 v[174:175], off
	v_lshl_add_u64 v[174:175], s[42:43], 0, v[2:3]
	s_mov_b32 m0, s44
	s_nop 0
	global_load_lds_dwordx4 v[174:175], off
	v_lshl_add_u64 v[174:175], s[42:43], 0, v[164:165]
	s_add_i32 m0, s44, 0x2000
	s_nop 0
	global_load_lds_dwordx4 v[174:175], off
	v_lshl_add_u64 v[174:175], v[186:187], 0, s[6:7]
	s_mov_b32 m0, s52
	s_nop 0
	global_load_lds_dwordx4 v[174:175], off
	v_lshl_add_u64 v[174:175], v[188:189], 0, s[6:7]
	s_mov_b32 m0, s53
	s_nop 0
	global_load_lds_dwordx4 v[174:175], off
	s_waitcnt vmcnt(8)
	s_waitcnt lgkmcnt(0)
	s_setprio 1
	s_barrier
	v_mfma_scale_f32_16x16x128_f8f6f4 v[96:99], v[4:11], v[196:203], v[96:99], v219, v220 op_sel_hi:[0,0,0]
	v_mfma_scale_f32_16x16x128_f8f6f4 v[92:95], v[12:19], v[196:203], v[92:95], v219, v220 op_sel_hi:[0,0,0]
	v_mfma_scale_f32_16x16x128_f8f6f4 v[88:91], v[4:11], v[204:211], v[88:91], v219, v220 op_sel_hi:[0,0,0]
	v_mfma_scale_f32_16x16x128_f8f6f4 v[84:87], v[12:19], v[204:211], v[84:87], v219, v220 op_sel_hi:[0,0,0]
	v_mfma_scale_f32_16x16x128_f8f6f4 v[72:75], v[4:11], v[226:233], v[72:75], v219, v220 op_sel_hi:[0,0,0]
	v_mfma_scale_f32_16x16x128_f8f6f4 v[68:71], v[12:19], v[226:233], v[68:71], v219, v220 op_sel_hi:[0,0,0]
	v_mfma_scale_f32_16x16x128_f8f6f4 v[56:59], v[4:11], v[234:241], v[56:59], v219, v220 op_sel_hi:[0,0,0]
	v_mfma_scale_f32_16x16x128_f8f6f4 v[52:55], v[12:19], v[234:241], v[52:55], v219, v220 op_sel_hi:[0,0,0]
	s_setprio 0
	s_setprio 1
	v_mfma_scale_f32_16x16x128_f8f6f4 v[80:83], v[20:27], v[196:203], v[80:83], v219, v220 op_sel_hi:[0,0,0]
	v_mfma_scale_f32_16x16x128_f8f6f4 v[76:79], v[28:35], v[196:203], v[76:79], v219, v220 op_sel_hi:[0,0,0]
	v_mfma_scale_f32_16x16x128_f8f6f4 v[64:67], v[20:27], v[204:211], v[64:67], v219, v220 op_sel_hi:[0,0,0]
	v_mfma_scale_f32_16x16x128_f8f6f4 v[60:63], v[28:35], v[204:211], v[60:63], v219, v220 op_sel_hi:[0,0,0]
	v_mfma_scale_f32_16x16x128_f8f6f4 v[48:51], v[20:27], v[226:233], v[48:51], v219, v220 op_sel_hi:[0,0,0]
	v_mfma_scale_f32_16x16x128_f8f6f4 v[44:47], v[28:35], v[226:233], v[44:47], v219, v220 op_sel_hi:[0,0,0]
	v_mfma_scale_f32_16x16x128_f8f6f4 v[40:43], v[20:27], v[234:241], v[40:43], v219, v220 op_sel_hi:[0,0,0]
	v_mfma_scale_f32_16x16x128_f8f6f4 v[36:39], v[28:35], v[234:241], v[36:39], v219, v220 op_sel_hi:[0,0,0]
	s_setprio 0
	s_barrier
	s_add_i32 s61, s61, 2
	s_add_u32 s40, s40, 0x100
	s_addc_u32 s41, s41, 0
	s_add_u32 s59, s59, 0x100
	s_addc_u32 s60, s60, 0
	s_cmp_gt_u32 s61, 41
	s_cbranch_scc0 .LBB0_1894
	s_nop 15
	s_nop 15
	s_and_b64 vcc, exec, s[36:37]
	s_cbranch_vccz .LBB0_1897
	s_barrier

.LBB0_1948:
	s_add_u32 s43, s44, 0xfffa8080
	s_addc_u32 s46, s45, -1
	s_add_i32 s42, 0, 0x10000
	s_cmp_eq_u32 s72, 18
	s_cselect_b32 s49, s5, s46
	s_cselect_b32 s48, s4, s43
	s_cselect_b32 s47, s41, s71
	s_cselect_b32 s46, s40, s70
	s_add_i32 s43, 0, 0x14000
	ds_read_b128 v[20:23], v190
	ds_read_b128 v[28:31], v190 offset:2048
	ds_read_b128 v[24:27], v190 offset:1024
	ds_read_b128 v[32:35], v190 offset:3072
	ds_read_b128 v[4:7], v190 offset:16384
	ds_read_b128 v[12:15], v190 offset:18432
	ds_read_b128 v[8:11], v190 offset:17408
	ds_read_b128 v[16:19], v190 offset:19456
	v_lshl_add_u64 v[174:175], s[44:45], 0, v[170:171]
	s_add_i32 m0, s59, 0xc000
	ds_read_b128 v[178:181], v193
	ds_read_b128 v[196:199], v193 offset:2048
	ds_read_b128 v[182:185], v194
	ds_read_b128 v[200:203], v194 offset:2048
	ds_read_b128 v[204:207], v193 offset:4096
	ds_read_b128 v[226:229], v193 offset:6144
	ds_read_b128 v[208:211], v194 offset:4096
	ds_read_b128 v[230:233], v194 offset:6144
	global_load_lds_dwordx4 v[174:175], off
	v_lshl_add_u64 v[174:175], s[44:45], 0, v[172:173]
	s_add_i32 m0, s59, 0xe000
	s_nop 0
	global_load_lds_dwordx4 v[174:175], off
	s_waitcnt vmcnt(8)
	s_waitcnt lgkmcnt(0)
	s_setprio 1
	s_barrier
	v_mfma_scale_f32_16x16x128_f8f6f4 v[160:163], v[20:27], v[178:185], v[160:163], v219, v220 op_sel_hi:[0,0,0]
	v_mfma_scale_f32_16x16x128_f8f6f4 v[156:159], v[28:35], v[178:185], v[156:159], v219, v220 op_sel_hi:[0,0,0]
	v_mfma_scale_f32_16x16x128_f8f6f4 v[152:155], v[20:27], v[196:203], v[152:155], v219, v220 op_sel_hi:[0,0,0]
	v_mfma_scale_f32_16x16x128_f8f6f4 v[148:151], v[28:35], v[196:203], v[148:151], v219, v220 op_sel_hi:[0,0,0]
	v_mfma_scale_f32_16x16x128_f8f6f4 v[136:139], v[20:27], v[204:211], v[136:139], v219, v220 op_sel_hi:[0,0,0]
	v_mfma_scale_f32_16x16x128_f8f6f4 v[132:135], v[28:35], v[204:211], v[132:135], v219, v220 op_sel_hi:[0,0,0]
	v_mfma_scale_f32_16x16x128_f8f6f4 v[120:123], v[20:27], v[226:233], v[120:123], v219, v220 op_sel_hi:[0,0,0]
	v_mfma_scale_f32_16x16x128_f8f6f4 v[116:119], v[28:35], v[226:233], v[116:119], v219, v220 op_sel_hi:[0,0,0]
	s_setprio 0
	s_setprio 1
	v_mfma_scale_f32_16x16x128_f8f6f4 v[144:147], v[4:11], v[178:185], v[144:147], v219, v220 op_sel_hi:[0,0,0]
	v_mfma_scale_f32_16x16x128_f8f6f4 v[140:143], v[12:19], v[178:185], v[140:143], v219, v220 op_sel_hi:[0,0,0]
	v_mfma_scale_f32_16x16x128_f8f6f4 v[128:131], v[4:11], v[196:203], v[128:131], v219, v220 op_sel_hi:[0,0,0]
	v_mfma_scale_f32_16x16x128_f8f6f4 v[124:127], v[12:19], v[196:203], v[124:127], v219, v220 op_sel_hi:[0,0,0]
	v_mfma_scale_f32_16x16x128_f8f6f4 v[112:115], v[4:11], v[204:211], v[112:115], v219, v220 op_sel_hi:[0,0,0]
	v_mfma_scale_f32_16x16x128_f8f6f4 v[108:111], v[12:19], v[204:211], v[108:111], v219, v220 op_sel_hi:[0,0,0]
	v_mfma_scale_f32_16x16x128_f8f6f4 v[104:107], v[4:11], v[226:233], v[104:107], v219, v220 op_sel_hi:[0,0,0]
	v_mfma_scale_f32_16x16x128_f8f6f4 v[100:103], v[12:19], v[226:233], v[100:103], v219, v220 op_sel_hi:[0,0,0]
	s_setprio 0
	s_barrier
	s_add_i32 s42, s42, s55
	v_lshl_add_u64 v[182:183], s[46:47], 0, v[2:3]
	s_mov_b32 m0, s42
	ds_read_b128 v[196:199], v193 offset:16384
	ds_read_b128 v[204:207], v193 offset:18432
	ds_read_b128 v[200:203], v194 offset:16384
	ds_read_b128 v[208:211], v194 offset:18432
	ds_read_b128 v[226:229], v193 offset:20480
	ds_read_b128 v[234:237], v193 offset:22528
	ds_read_b128 v[230:233], v194 offset:20480
	ds_read_b128 v[238:241], v194 offset:22528
	global_load_lds_dwordx4 v[182:183], off
	s_add_i32 m0, s42, 0x2000
	s_add_u32 s74, s46, 0x58000
	v_lshl_add_u64 v[184:185], s[46:47], 0, v[164:165]
	s_addc_u32 s75, s47, 0
	s_add_i32 s42, s43, s55
	global_load_lds_dwordx4 v[184:185], off
	v_lshl_add_u64 v[174:175], s[74:75], 0, v[2:3]
	s_mov_b32 m0, s42
	v_lshl_add_u64 v[186:187], s[48:49], 0, v[168:169]
	global_load_lds_dwordx4 v[174:175], off
	v_lshl_add_u64 v[174:175], s[74:75], 0, v[164:165]
	s_add_i32 m0, s42, 0x2000
	v_lshl_add_u64 v[188:189], s[48:49], 0, v[166:167]
	global_load_lds_dwordx4 v[174:175], off
	s_mov_b32 m0, s59
	s_nop 0
	global_load_lds_dwordx4 v[186:187], off
	s_mov_b32 m0, s60
	s_nop 0
	global_load_lds_dwordx4 v[188:189], off
	s_waitcnt vmcnt(8)
	s_waitcnt lgkmcnt(0)
	s_setprio 1
	s_barrier
	v_mfma_scale_f32_16x16x128_f8f6f4 v[96:99], v[20:27], v[196:203], v[96:99], v219, v220 op_sel_hi:[0,0,0]
	v_mfma_scale_f32_16x16x128_f8f6f4 v[92:95], v[28:35], v[196:203], v[92:95], v219, v220 op_sel_hi:[0,0,0]
	v_mfma_scale_f32_16x16x128_f8f6f4 v[88:91], v[20:27], v[204:211], v[88:91], v219, v220 op_sel_hi:[0,0,0]
	v_mfma_scale_f32_16x16x128_f8f6f4 v[84:87], v[28:35], v[204:211], v[84:87], v219, v220 op_sel_hi:[0,0,0]
	v_mfma_scale_f32_16x16x128_f8f6f4 v[72:75], v[20:27], v[226:233], v[72:75], v219, v220 op_sel_hi:[0,0,0]
	v_mfma_scale_f32_16x16x128_f8f6f4 v[68:71], v[28:35], v[226:233], v[68:71], v219, v220 op_sel_hi:[0,0,0]
	v_mfma_scale_f32_16x16x128_f8f6f4 v[56:59], v[20:27], v[234:241], v[56:59], v219, v220 op_sel_hi:[0,0,0]
	v_mfma_scale_f32_16x16x128_f8f6f4 v[52:55], v[28:35], v[234:241], v[52:55], v219, v220 op_sel_hi:[0,0,0]
	s_setprio 0
	s_setprio 1
	v_mfma_scale_f32_16x16x128_f8f6f4 v[80:83], v[4:11], v[196:203], v[80:83], v219, v220 op_sel_hi:[0,0,0]
	v_mfma_scale_f32_16x16x128_f8f6f4 v[76:79], v[12:19], v[196:203], v[76:79], v219, v220 op_sel_hi:[0,0,0]
	v_mfma_scale_f32_16x16x128_f8f6f4 v[64:67], v[4:11], v[204:211], v[64:67], v219, v220 op_sel_hi:[0,0,0]
	v_mfma_scale_f32_16x16x128_f8f6f4 v[60:63], v[12:19], v[204:211], v[60:63], v219, v220 op_sel_hi:[0,0,0]
	v_mfma_scale_f32_16x16x128_f8f6f4 v[48:51], v[4:11], v[226:233], v[48:51], v219, v220 op_sel_hi:[0,0,0]
	v_mfma_scale_f32_16x16x128_f8f6f4 v[44:47], v[12:19], v[226:233], v[44:47], v219, v220 op_sel_hi:[0,0,0]
	v_mfma_scale_f32_16x16x128_f8f6f4 v[40:43], v[4:11], v[234:241], v[40:43], v219, v220 op_sel_hi:[0,0,0]
	v_mfma_scale_f32_16x16x128_f8f6f4 v[36:39], v[12:19], v[234:241], v[36:39], v219, v220 op_sel_hi:[0,0,0]
	s_setprio 0
	s_barrier
	s_add_i32 s73, 0, 0x18000
	s_add_i32 s74, 0, 0x1c000
	ds_read_b128 v[4:7], v190 offset:32768
	ds_read_b128 v[12:15], v190 offset:34816
	ds_read_b128 v[8:11], v190 offset:33792
	ds_read_b128 v[16:19], v190 offset:35840
	ds_read_b128 v[20:23], v190 offset:49152
	ds_read_b128 v[28:31], v190 offset:51200
	ds_read_b128 v[24:27], v190 offset:50176
	ds_read_b128 v[32:35], v190 offset:52224
	s_add_u32 s42, s48, 0x58000
	s_addc_u32 s43, s49, 0
	s_mov_b32 m0, s61
	v_lshl_add_u64 v[174:175], s[42:43], 0, v[168:169]
	ds_read_b128 v[196:199], v193 offset:32768
	ds_read_b128 v[204:207], v193 offset:34816
	ds_read_b128 v[200:203], v194 offset:32768
	ds_read_b128 v[208:211], v194 offset:34816
	ds_read_b128 v[226:229], v193 offset:36864
	ds_read_b128 v[234:237], v193 offset:38912
	ds_read_b128 v[230:233], v194 offset:36864
	ds_read_b128 v[238:241], v194 offset:38912
	global_load_lds_dwordx4 v[174:175], off
	v_lshl_add_u64 v[174:175], s[42:43], 0, v[166:167]
	s_mov_b32 m0, s62
	s_nop 0
	global_load_lds_dwordx4 v[174:175], off
	s_waitcnt vmcnt(8)
	s_waitcnt lgkmcnt(0)
	s_setprio 1
	s_barrier
	v_mfma_scale_f32_16x16x128_f8f6f4 v[160:163], v[4:11], v[196:203], v[160:163], v219, v220 op_sel_hi:[0,0,0]
	v_mfma_scale_f32_16x16x128_f8f6f4 v[156:159], v[12:19], v[196:203], v[156:159], v219, v220 op_sel_hi:[0,0,0]
	v_mfma_scale_f32_16x16x128_f8f6f4 v[152:155], v[4:11], v[204:211], v[152:155], v219, v220 op_sel_hi:[0,0,0]
	v_mfma_scale_f32_16x16x128_f8f6f4 v[148:151], v[12:19], v[204:211], v[148:151], v219, v220 op_sel_hi:[0,0,0]
	v_mfma_scale_f32_16x16x128_f8f6f4 v[136:139], v[4:11], v[226:233], v[136:139], v219, v220 op_sel_hi:[0,0,0]
	v_mfma_scale_f32_16x16x128_f8f6f4 v[132:135], v[12:19], v[226:233], v[132:135], v219, v220 op_sel_hi:[0,0,0]
	v_mfma_scale_f32_16x16x128_f8f6f4 v[120:123], v[4:11], v[234:241], v[120:123], v219, v220 op_sel_hi:[0,0,0]
	v_mfma_scale_f32_16x16x128_f8f6f4 v[116:119], v[12:19], v[234:241], v[116:119], v219, v220 op_sel_hi:[0,0,0]
	s_setprio 0
	s_setprio 1
	v_mfma_scale_f32_16x16x128_f8f6f4 v[144:147], v[20:27], v[196:203], v[144:147], v219, v220 op_sel_hi:[0,0,0]
	v_mfma_scale_f32_16x16x128_f8f6f4 v[140:143], v[28:35], v[196:203], v[140:143], v219, v220 op_sel_hi:[0,0,0]
	v_mfma_scale_f32_16x16x128_f8f6f4 v[128:131], v[20:27], v[204:211], v[128:131], v219, v220 op_sel_hi:[0,0,0]
	v_mfma_scale_f32_16x16x128_f8f6f4 v[124:127], v[28:35], v[204:211], v[124:127], v219, v220 op_sel_hi:[0,0,0]
	v_mfma_scale_f32_16x16x128_f8f6f4 v[112:115], v[20:27], v[226:233], v[112:115], v219, v220 op_sel_hi:[0,0,0]
	v_mfma_scale_f32_16x16x128_f8f6f4 v[108:111], v[28:35], v[226:233], v[108:111], v219, v220 op_sel_hi:[0,0,0]
	v_mfma_scale_f32_16x16x128_f8f6f4 v[104:107], v[20:27], v[234:241], v[104:107], v219, v220 op_sel_hi:[0,0,0]
	v_mfma_scale_f32_16x16x128_f8f6f4 v[100:103], v[28:35], v[234:241], v[100:103], v219, v220 op_sel_hi:[0,0,0]
	s_setprio 0
	s_barrier
	s_add_i32 s42, s73, s55
	v_lshl_add_u64 v[174:175], v[182:183], 0, s[6:7]
	s_mov_b32 m0, s42
	ds_read_b128 v[196:199], v193 offset:49152
	ds_read_b128 v[204:207], v193 offset:51200
	ds_read_b128 v[200:203], v194 offset:49152
	ds_read_b128 v[208:211], v194 offset:51200
	ds_read_b128 v[226:229], v193 offset:53248
	ds_read_b128 v[234:237], v193 offset:55296
	ds_read_b128 v[230:233], v194 offset:53248
	ds_read_b128 v[238:241], v194 offset:55296
	global_load_lds_dwordx4 v[174:175], off
	s_add_i32 m0, s42, 0x2000
	s_add_u32 s42, s46, 0x58080
	v_lshl_add_u64 v[174:175], v[184:185], 0, s[6:7]
	s_addc_u32 s43, s47, 0
	s_add_i32 s46, s74, s55
	global_load_lds_dwordx4 v[174:175], off
	v_lshl_add_u64 v[174:175], s[42:43], 0, v[2:3]
	s_mov_b32 m0, s46
	s_nop 0
	global_load_lds_dwordx4 v[174:175], off
	v_lshl_add_u64 v[174:175], s[42:43], 0, v[164:165]
	s_add_i32 m0, s46, 0x2000
	s_nop 0
	global_load_lds_dwordx4 v[174:175], off
	v_lshl_add_u64 v[174:175], v[186:187], 0, s[6:7]
	s_mov_b32 m0, s64
	s_nop 0
	global_load_lds_dwordx4 v[174:175], off
	v_lshl_add_u64 v[174:175], v[188:189], 0, s[6:7]
	s_mov_b32 m0, s65
	s_nop 0
	global_load_lds_dwordx4 v[174:175], off
	s_waitcnt vmcnt(8)
	s_waitcnt lgkmcnt(0)
	s_setprio 1
	s_barrier
	v_mfma_scale_f32_16x16x128_f8f6f4 v[96:99], v[4:11], v[196:203], v[96:99], v219, v220 op_sel_hi:[0,0,0]
	v_mfma_scale_f32_16x16x128_f8f6f4 v[92:95], v[12:19], v[196:203], v[92:95], v219, v220 op_sel_hi:[0,0,0]
	v_mfma_scale_f32_16x16x128_f8f6f4 v[88:91], v[4:11], v[204:211], v[88:91], v219, v220 op_sel_hi:[0,0,0]
	v_mfma_scale_f32_16x16x128_f8f6f4 v[84:87], v[12:19], v[204:211], v[84:87], v219, v220 op_sel_hi:[0,0,0]
	v_mfma_scale_f32_16x16x128_f8f6f4 v[72:75], v[4:11], v[226:233], v[72:75], v219, v220 op_sel_hi:[0,0,0]
	v_mfma_scale_f32_16x16x128_f8f6f4 v[68:71], v[12:19], v[226:233], v[68:71], v219, v220 op_sel_hi:[0,0,0]
	v_mfma_scale_f32_16x16x128_f8f6f4 v[56:59], v[4:11], v[234:241], v[56:59], v219, v220 op_sel_hi:[0,0,0]
	v_mfma_scale_f32_16x16x128_f8f6f4 v[52:55], v[12:19], v[234:241], v[52:55], v219, v220 op_sel_hi:[0,0,0]
	s_setprio 0
	s_setprio 1
	v_mfma_scale_f32_16x16x128_f8f6f4 v[80:83], v[20:27], v[196:203], v[80:83], v219, v220 op_sel_hi:[0,0,0]
	v_mfma_scale_f32_16x16x128_f8f6f4 v[76:79], v[28:35], v[196:203], v[76:79], v219, v220 op_sel_hi:[0,0,0]
	v_mfma_scale_f32_16x16x128_f8f6f4 v[64:67], v[20:27], v[204:211], v[64:67], v219, v220 op_sel_hi:[0,0,0]
	v_mfma_scale_f32_16x16x128_f8f6f4 v[60:63], v[28:35], v[204:211], v[60:63], v219, v220 op_sel_hi:[0,0,0]
	v_mfma_scale_f32_16x16x128_f8f6f4 v[48:51], v[20:27], v[226:233], v[48:51], v219, v220 op_sel_hi:[0,0,0]
	v_mfma_scale_f32_16x16x128_f8f6f4 v[44:47], v[28:35], v[226:233], v[44:47], v219, v220 op_sel_hi:[0,0,0]
	v_mfma_scale_f32_16x16x128_f8f6f4 v[40:43], v[20:27], v[234:241], v[40:43], v219, v220 op_sel_hi:[0,0,0]
	v_mfma_scale_f32_16x16x128_f8f6f4 v[36:39], v[28:35], v[234:241], v[36:39], v219, v220 op_sel_hi:[0,0,0]
	s_setprio 0
	s_barrier
	s_add_i32 s72, s72, 2
	s_add_u32 s44, s44, 0x100
	s_addc_u32 s45, s45, 0
	s_add_u32 s70, s70, 0x100
	s_addc_u32 s71, s71, 0
	s_cmp_gt_u32 s72, 19
	s_cbranch_scc0 .LBB0_1948
	s_nop 15
	s_nop 15
	s_and_b64 vcc, exec, s[38:39]
	s_cbranch_vccz .LBB0_1951
	s_barrier
